# weight conversion items remapped so that a workgroup's eight waves cover consecutive k blocks of one column block (contiguous 512-byte destination rows); attention loop reschedule kept
# speedup vs baseline: 1.0071x; 1.0038x over previous
; #define LAS __attribute__((address_space(3)))
; __device__ __forceinline__ unsigned pk4_fp8(float x0, float x1, float x2, float x3) { int w = 0; w = __builtin_amdgcn_cvt_pk_fp8_f32(x0, x1, w, false); w = __builtin_amdgcn_cvt_pk_fp8_f32(x2, x3, w, true); return (unsigned)w; }
; __device__ __forceinline__ void transpose_item_fp8w(const float* W, int K, int N, unsigned char* WT, float q, LAS unsigned char* scr, int item, int lane) {
;     const int nblk = N / 128, kb = item / nblk, nb = item % nblk, k0 = 64 * kb, n0 = 128 * nb;
;     const int l5 = lane & 31, h = lane >> 5;
;     const float* src = W + (size_t)(k0 + 16 * h) * N + n0 + 4 * l5;
; #pragma unroll
;     for (int b = 0; b < 2; ++b) {
;         f32x4 x[16];
; #pragma unroll
;         for (int s_ = 0; s_ < 16; ++s_) x[s_] = *(const f32x4*)(src + (size_t)(32 * b + s_) * N);
; #pragma unroll
;         for (int i = 0; i < 4; ++i) {
;             u32x4 o;
;             o.x = pk4_fp8(x[0][i] * q, x[1][i] * q, x[2][i] * q, x[3][i] * q); o.y = pk4_fp8(x[4][i] * q, x[5][i] * q, x[6][i] * q, x[7][i] * q);
;             o.z = pk4_fp8(x[8][i] * q, x[9][i] * q, x[10][i] * q, x[11][i] * q); o.w = pk4_fp8(x[12][i] * q, x[13][i] * q, x[14][i] * q, x[15][i] * q);
;             *(LAS u32x4*)(scr + (l5 + 32 * i) * 80 + (2 * b + h) * 16) = o; }
.LBB0_38:
	s_cmpk_gt_i32 s66, 0x3df
	s_mov_b64 s[6:7], -1
	s_cbranch_scc0 .LBB0_70
	s_cmpk_gt_u32 s66, 0x46f
	s_cbranch_scc0 .LBB0_57
	s_cmpk_gt_u32 s66, 0x4ef
	s_cbranch_scc0 .LBB0_52
	s_cmpk_gt_u32 s66, 0x6ef
	s_cbranch_scc0 .LBB0_47
	s_cmpk_gt_u32 s66, 0x26ef
	v_lshlrev_b32_e32 v142, 2, v140
	v_add_u32_e32 v195, v179, v180
	s_cbranch_scc0 .LBB0_44
	s_add_i32 s67, s66, 0xffffd910
	s_lshr_b32 s4, s67, 7
	s_lshl_b64 s[8:9], s[4:5], 20
	s_lshl_b64 s[6:7], s[4:5], 22
	s_add_u32 s68, s16, s6
	s_addc_u32 s69, s17, s7
	v_readlane_b32 s4, v246, 17
	s_add_u32 s7, s4, s8
	v_readlane_b32 s4, v246, 18
	s_addc_u32 s8, s4, s9
	s_lshl_b32 s4, s67, 6
	s_and_b32 s9, s4, 0x3c0
	v_add_u32_e32 v0, s9, v177
	s_lshl_b32 s4, s67, 3
	v_ashrrev_i32_e32 v1, 31, v0
	s_and_b32 s6, s4, 0x380
	v_lshlrev_b64 v[0:1], 12, v[0:1]
	v_lshl_add_u64 v[0:1], s[68:69], 0, v[0:1]
	s_lshl_b32 s4, s6, 2
	v_lshl_add_u64 v[0:1], v[0:1], 0, s[4:5]
	v_lshl_add_u64 v[80:81], v[0:1], 0, v[142:143]
	v_add_co_u32_e32 v8, vcc, s10, v80
	global_load_dwordx4 v[0:3], v[80:81], off
	s_nop 0
	v_addc_co_u32_e32 v9, vcc, 0, v81, vcc
	v_add_co_u32_e32 v12, vcc, s11, v80
	global_load_dwordx4 v[4:7], v[8:9], off offset:-4096
	s_nop 0
	global_load_dwordx4 v[8:11], v[8:9], off
	v_addc_co_u32_e32 v13, vcc, 0, v81, vcc
	v_add_co_u32_e32 v16, vcc, s15, v80
	global_load_dwordx4 v[20:23], v[12:13], off offset:-4096
	s_nop 0
	global_load_dwordx4 v[12:15], v[12:13], off
	v_addc_co_u32_e32 v17, vcc, 0, v81, vcc
	v_add_co_u32_e32 v28, vcc, s20, v80
	global_load_dwordx4 v[24:27], v[16:17], off offset:-4096
	s_nop 0
	global_load_dwordx4 v[16:19], v[16:17], off
	v_addc_co_u32_e32 v29, vcc, 0, v81, vcc
	v_add_co_u32_e32 v40, vcc, s21, v80
	global_load_dwordx4 v[32:35], v[28:29], off offset:-4096
	s_nop 0
	global_load_dwordx4 v[28:31], v[28:29], off
	v_addc_co_u32_e32 v41, vcc, 0, v81, vcc
	v_add_co_u32_e32 v44, vcc, s22, v80
	global_load_dwordx4 v[36:39], v[40:41], off offset:-4096
	s_nop 0
	global_load_dwordx4 v[40:43], v[40:41], off
	v_addc_co_u32_e32 v45, vcc, 0, v81, vcc
	v_add_co_u32_e32 v48, vcc, s23, v80
	global_load_dwordx4 v[52:55], v[44:45], off offset:-4096
	s_nop 0
	global_load_dwordx4 v[44:47], v[44:45], off
	v_addc_co_u32_e32 v49, vcc, 0, v81, vcc
	global_load_dwordx4 v[56:59], v[48:49], off offset:-4096
	s_nop 0
	global_load_dwordx4 v[48:51], v[48:49], off
	v_add_co_u32_e32 v60, vcc, s24, v80
	v_mov_b32_e32 v64, v143
	s_nop 0
	v_addc_co_u32_e32 v61, vcc, 0, v81, vcc
	global_load_dwordx4 v[60:63], v[60:61], off
	v_mov_b32_e32 v68, v143
	v_mov_b32_e32 v69, v143
	v_mov_b32_e32 v70, v143
	v_mov_b32_e32 v71, v143
	v_mov_b32_e32 v136, v143
	v_mov_b32_e32 v137, v143
	v_mov_b32_e32 v138, v143
	v_mov_b32_e32 v139, v143
	v_mov_b32_e32 v65, v143
	v_mov_b32_e32 v66, v143
	v_mov_b32_e32 v67, v143
	s_add_u32 s68, s7, s9
	s_addc_u32 s69, s8, 0
	s_waitcnt vmcnt(15)
	v_mul_f32_e32 v0, 0x43800000, v0
	v_mul_f32_e32 v1, 0x43800000, v1
	s_waitcnt vmcnt(14)
	v_mul_f32_e32 v4, 0x43800000, v4
	v_mul_f32_e32 v5, 0x43800000, v5
	v_cvt_pk_fp8_f32 v64, v0, v4
	v_cvt_pk_fp8_f32 v68, v1, v5
	s_waitcnt vmcnt(13)
	v_mul_f32_e32 v8, 0x43800000, v8
	s_waitcnt vmcnt(12)
	v_mul_f32_e32 v20, 0x43800000, v20
	s_waitcnt vmcnt(11)
	v_mul_f32_e32 v0, 0x43800000, v13
	v_mul_f32_e32 v12, 0x43800000, v12
	v_mul_f32_e32 v9, 0x43800000, v9
	v_mul_f32_e32 v21, 0x43800000, v21
	s_waitcnt vmcnt(10)
	v_mul_f32_e32 v1, 0x43800000, v25
	v_cvt_pk_fp8_f32 v69, v0, v1
	s_waitcnt vmcnt(9)
	v_mul_f32_e32 v0, 0x43800000, v17
	v_mul_f32_e32 v24, 0x43800000, v24
	v_cvt_pk_fp8_f32 v65, v12, v24
	s_waitcnt vmcnt(8)
	v_mul_f32_e32 v1, 0x43800000, v33
	v_cvt_pk_fp8_f32 v69, v0, v1 op_sel:[0,0,1]
	s_waitcnt vmcnt(7)
	v_mul_f32_e32 v0, 0x43800000, v29
	v_mul_f32_e32 v28, 0x43800000, v28
	v_mul_f32_e32 v16, 0x43800000, v16
	s_waitcnt vmcnt(6)
	v_mul_f32_e32 v1, 0x43800000, v37
	v_cvt_pk_fp8_f32 v70, v0, v1
	s_waitcnt vmcnt(5)
	v_mul_f32_e32 v4, 0x43800000, v41
	v_mul_f32_e32 v36, 0x43800000, v36
	v_cvt_pk_fp8_f32 v66, v28, v36
	s_waitcnt vmcnt(4)
	v_mul_f32_e32 v5, 0x43800000, v53
	s_waitcnt vmcnt(3)
	v_mul_f32_e32 v0, 0x43800000, v45
	v_cvt_pk_fp8_f32 v70, v4, v5 op_sel:[0,0,1]
	s_waitcnt vmcnt(2)
	v_mul_f32_e32 v1, 0x43800000, v57
	v_cvt_pk_fp8_f32 v71, v0, v1
	s_waitcnt vmcnt(1)
	v_mul_f32_e32 v0, 0x43800000, v49
	v_mul_f32_e32 v5, 0x43800000, v14
	v_mul_f32_e32 v4, 0x43800000, v22
	v_mul_f32_e32 v44, 0x43800000, v44
	v_mul_f32_e32 v56, 0x43800000, v56
	s_waitcnt vmcnt(0)
; #define LAS __attribute__((address_space(3)))
; __device__ __forceinline__ unsigned pk4_fp8(float x0, float x1, float x2, float x3) { int w = 0; w = __builtin_amdgcn_cvt_pk_fp8_f32(x0, x1, w, false); w = __builtin_amdgcn_cvt_pk_fp8_f32(x2, x3, w, true); return (unsigned)w; }
; __device__ __forceinline__ void transpose_item_fp8w(const float* W, int K, int N, unsigned char* WT, float q, LAS unsigned char* scr, int item, int lane) {
;     ...
;     for (int b = 0; b < 2; ++b) {
;         f32x4 x[16];
; #pragma unroll
;         for (int s_ = 0; s_ < 16; ++s_) x[s_] = *(const f32x4*)(src + (size_t)(32 * b + s_) * N);
; #pragma unroll
;         for (int i = 0; i < 4; ++i) {
;             u32x4 o;
;             o.x = pk4_fp8(x[0][i] * q, x[1][i] * q, x[2][i] * q, x[3][i] * q); o.y = pk4_fp8(x[4][i] * q, x[5][i] * q, x[6][i] * q, x[7][i] * q);
;             o.z = pk4_fp8(x[8][i] * q, x[9][i] * q, x[10][i] * q, x[11][i] * q); o.w = pk4_fp8(x[12][i] * q, x[13][i] * q, x[14][i] * q, x[15][i] * q);
;             *(LAS u32x4*)(scr + (l5 + 32 * i) * 80 + (2 * b + h) * 16) = o; }
	v_mul_f32_e32 v1, 0x43800000, v61
	v_cvt_pk_fp8_f32 v71, v0, v1 op_sel:[0,0,1]
	v_mul_f32_e32 v0, 0x43800000, v2
	v_mul_f32_e32 v1, 0x43800000, v6
	v_cvt_pk_fp8_f32 v136, v0, v1
	v_add_co_u32_e32 v0, vcc, s25, v80
	v_mul_f32_e32 v2, 0x43800000, v10
	s_nop 0
	v_addc_co_u32_e32 v1, vcc, 0, v81, vcc
	global_load_dwordx4 v[88:91], v[0:1], off offset:-4096
	global_load_dwordx4 v[92:95], v[0:1], off
	v_add_co_u32_e32 v0, vcc, s26, v80
	v_cvt_pk_fp8_f32 v136, v2, v4 op_sel:[0,0,1]
	s_nop 0
	v_addc_co_u32_e32 v1, vcc, 0, v81, vcc
	global_load_dwordx4 v[128:131], v[0:1], off offset:-4096
	global_load_dwordx4 v[132:135], v[0:1], off
	v_add_co_u32_e32 v0, vcc, s27, v80
	v_mul_f32_e32 v2, 0x43800000, v42
	s_nop 0
	v_addc_co_u32_e32 v1, vcc, 0, v81, vcc
	global_load_dwordx4 v[112:115], v[0:1], off offset:-4096
	global_load_dwordx4 v[116:119], v[0:1], off
	v_add_co_u32_e32 v0, vcc, s28, v80
	v_mul_f32_e32 v4, 0x43800000, v54
	s_nop 0
	v_addc_co_u32_e32 v1, vcc, 0, v81, vcc
	global_load_dwordx4 v[96:99], v[0:1], off offset:-4096
	global_load_dwordx4 v[100:103], v[0:1], off
	v_add_co_u32_e32 v0, vcc, s29, v80
	v_cvt_pk_fp8_f32 v67, v44, v56
	s_nop 0
	v_addc_co_u32_e32 v1, vcc, 0, v81, vcc
	global_load_dwordx4 v[72:75], v[0:1], off offset:-4096
	global_load_dwordx4 v[76:79], v[0:1], off
	v_add_co_u32_e32 v0, vcc, s30, v80
	v_mul_f32_e32 v32, 0x43800000, v32
	s_nop 0
	v_addc_co_u32_e32 v1, vcc, 0, v81, vcc
	global_load_dwordx4 v[120:123], v[0:1], off offset:-4096
	global_load_dwordx4 v[124:127], v[0:1], off
	v_add_co_u32_e32 v0, vcc, s31, v80
	v_mul_f32_e32 v40, 0x43800000, v40
	s_nop 0
	v_addc_co_u32_e32 v1, vcc, 0, v81, vcc
	global_load_dwordx4 v[104:107], v[0:1], off offset:-4096
	global_load_dwordx4 v[108:111], v[0:1], off
	v_add_co_u32_e32 v0, vcc, s33, v80
	v_mul_f32_e32 v52, 0x43800000, v52
	s_nop 0
	v_addc_co_u32_e32 v1, vcc, 0, v81, vcc
	global_load_dwordx4 v[80:83], v[0:1], off offset:-4096
	global_load_dwordx4 v[84:87], v[0:1], off
	v_mul_f32_e32 v0, 0x43800000, v26
	v_cvt_pk_fp8_f32 v137, v5, v0
	v_mul_f32_e32 v0, 0x43800000, v18
	v_mul_f32_e32 v1, 0x43800000, v34
	v_mul_f32_e32 v5, 0x43800000, v27
	v_cvt_pk_fp8_f32 v137, v0, v1 op_sel:[0,0,1]
	v_mul_f32_e32 v0, 0x43800000, v30
	v_mul_f32_e32 v1, 0x43800000, v38
	v_cvt_pk_fp8_f32 v138, v0, v1
	v_mul_f32_e32 v0, 0x43800000, v46
	v_mul_f32_e32 v1, 0x43800000, v58
	v_cvt_pk_fp8_f32 v139, v0, v1
	v_mul_f32_e32 v0, 0x43800000, v50
	v_mul_f32_e32 v1, 0x43800000, v62
	v_cvt_pk_fp8_f32 v138, v2, v4 op_sel:[0,0,1]
	v_cvt_pk_fp8_f32 v139, v0, v1 op_sel:[0,0,1]
	v_mul_f32_e32 v1, 0x43800000, v3
	v_mul_f32_e32 v2, 0x43800000, v7
	v_mov_b32_e32 v0, v143
	v_cvt_pk_fp8_f32 v0, v1, v2
	v_mul_f32_e32 v2, 0x43800000, v15
	v_mov_b32_e32 v1, v143
	v_cvt_pk_fp8_f32 v1, v2, v5
	v_mul_f32_e32 v3, 0x43800000, v11
	v_mul_f32_e32 v4, 0x43800000, v23
	v_cvt_pk_fp8_f32 v0, v3, v4 op_sel:[0,0,1]
	v_mul_f32_e32 v2, 0x43800000, v19
	v_mul_f32_e32 v3, 0x43800000, v35
	v_cvt_pk_fp8_f32 v1, v2, v3 op_sel:[0,0,1]
	v_mul_f32_e32 v3, 0x43800000, v31
	v_mul_f32_e32 v4, 0x43800000, v39
	v_mov_b32_e32 v2, v143
	v_cvt_pk_fp8_f32 v2, v3, v4
	v_mul_f32_e32 v4, 0x43800000, v47
	v_mul_f32_e32 v7, 0x43800000, v59
	v_mov_b32_e32 v3, v143
	v_mul_f32_e32 v48, 0x43800000, v48
	v_mul_f32_e32 v60, 0x43800000, v60
	v_cvt_pk_fp8_f32 v3, v4, v7
	v_cvt_pk_fp8_f32 v64, v8, v20 op_sel:[0,0,1]
	v_cvt_pk_fp8_f32 v65, v16, v32 op_sel:[0,0,1]
	v_cvt_pk_fp8_f32 v66, v40, v52 op_sel:[0,0,1]
	v_cvt_pk_fp8_f32 v67, v48, v60 op_sel:[0,0,1]
	v_cvt_pk_fp8_f32 v68, v9, v21 op_sel:[0,0,1]
	v_mul_f32_e32 v5, 0x43800000, v43
	v_mul_f32_e32 v6, 0x43800000, v55
	v_cvt_pk_fp8_f32 v2, v5, v6 op_sel:[0,0,1]
	v_mul_f32_e32 v4, 0x43800000, v51
	v_mul_f32_e32 v5, 0x43800000, v63
	v_cvt_pk_fp8_f32 v3, v4, v5 op_sel:[0,0,1]
	ds_write_b128 v194, v[64:67]
	ds_write_b128 v194, v[68:71] offset:2560
	ds_write_b128 v194, v[136:139] offset:5120
	ds_write_b128 v194, v[0:3] offset:7680
	s_waitcnt vmcnt(15)
	v_mul_f32_e32 v1, 0x43800000, v88
	s_waitcnt vmcnt(14)
	v_mul_f32_e32 v2, 0x43800000, v92
	v_mov_b32_e32 v0, v143
	v_cvt_pk_fp8_f32 v0, v1, v2
	s_waitcnt vmcnt(11)
	v_mul_f32_e32 v2, 0x43800000, v112
	s_waitcnt vmcnt(10)
	v_mul_f32_e32 v5, 0x43800000, v116
	v_mov_b32_e32 v1, v143
	v_cvt_pk_fp8_f32 v1, v2, v5
	v_mul_f32_e32 v3, 0x43800000, v128
	v_mul_f32_e32 v4, 0x43800000, v132
	v_cvt_pk_fp8_f32 v0, v3, v4 op_sel:[0,0,1]
	s_waitcnt vmcnt(9)
	v_mul_f32_e32 v2, 0x43800000, v96
	s_waitcnt vmcnt(8)
	v_mul_f32_e32 v3, 0x43800000, v100
	v_cvt_pk_fp8_f32 v1, v2, v3 op_sel:[0,0,1]
	s_waitcnt vmcnt(7)
	v_mul_f32_e32 v3, 0x43800000, v72
	s_waitcnt vmcnt(6)
	v_mul_f32_e32 v4, 0x43800000, v76
	v_mov_b32_e32 v2, v143
	v_cvt_pk_fp8_f32 v2, v3, v4
	v_mov_b32_e32 v3, v143
	s_waitcnt vmcnt(5)
	v_mul_f32_e32 v5, 0x43800000, v120
	s_waitcnt vmcnt(4)
	v_mul_f32_e32 v6, 0x43800000, v124
	s_waitcnt vmcnt(3)
	v_mul_f32_e32 v4, 0x43800000, v104
	s_waitcnt vmcnt(2)
	v_mul_f32_e32 v7, 0x43800000, v108
	v_cvt_pk_fp8_f32 v3, v4, v7
	v_cvt_pk_fp8_f32 v2, v5, v6 op_sel:[0,0,1]
	v_mul_f32_e32 v6, 0x43800000, v93
	v_mul_f32_e32 v9, 0x43800000, v117
	s_waitcnt vmcnt(1)
	v_mul_f32_e32 v4, 0x43800000, v80
	s_waitcnt vmcnt(0)
; #define LAS __attribute__((address_space(3)))
; __device__ __forceinline__ unsigned pk4_fp8(float x0, float x1, float x2, float x3) { int w = 0; w = __builtin_amdgcn_cvt_pk_fp8_f32(x0, x1, w, false); w = __builtin_amdgcn_cvt_pk_fp8_f32(x2, x3, w, true); return (unsigned)w; }
; __device__ __forceinline__ void transpose_item_fp8w(const float* W, int K, int N, unsigned char* WT, float q, LAS unsigned char* scr, int item, int lane) {
;     ...
; #pragma unroll
;         for (int i = 0; i < 4; ++i) {
;             u32x4 o;
;             o.x = pk4_fp8(x[0][i] * q, x[1][i] * q, x[2][i] * q, x[3][i] * q); o.y = pk4_fp8(x[4][i] * q, x[5][i] * q, x[6][i] * q, x[7][i] * q);
;             o.z = pk4_fp8(x[8][i] * q, x[9][i] * q, x[10][i] * q, x[11][i] * q); o.w = pk4_fp8(x[12][i] * q, x[13][i] * q, x[14][i] * q, x[15][i] * q);
;             *(LAS u32x4*)(scr + (l5 + 32 * i) * 80 + (2 * b + h) * 16) = o; }
;     }
;     asm volatile("s_waitcnt lgkmcnt(0)" ::: "memory");
; #pragma unroll
;     for (int qd = 0; qd < 8; ++qd) {
;         const int rho = 16 * qd + (lane >> 2), piece = lane & 3;
;         const u32x4 o = *(const LAS u32x4*)(scr + rho * 80 + piece * 16);
;         const int nl = 4 * (rho & 31) + (rho >> 5);
;         *(u32x4*)(WT + (size_t)(n0 + nl) * K + k0 + piece * 16) = o; }
;     asm volatile("s_waitcnt lgkmcnt(0)" ::: "memory");
	v_mul_f32_e32 v5, 0x43800000, v84
	v_cvt_pk_fp8_f32 v3, v4, v5 op_sel:[0,0,1]
	v_mul_f32_e32 v5, 0x43800000, v89
	v_mov_b32_e32 v4, v143
	v_cvt_pk_fp8_f32 v4, v5, v6
	v_mul_f32_e32 v6, 0x43800000, v113
	v_mov_b32_e32 v5, v143
	v_cvt_pk_fp8_f32 v5, v6, v9
	v_mul_f32_e32 v7, 0x43800000, v129
	v_mul_f32_e32 v8, 0x43800000, v133
	v_cvt_pk_fp8_f32 v4, v7, v8 op_sel:[0,0,1]
	v_mul_f32_e32 v6, 0x43800000, v97
	v_mul_f32_e32 v7, 0x43800000, v101
	v_cvt_pk_fp8_f32 v5, v6, v7 op_sel:[0,0,1]
	v_mul_f32_e32 v7, 0x43800000, v73
	v_mul_f32_e32 v8, 0x43800000, v77
	v_mov_b32_e32 v6, v143
	v_cvt_pk_fp8_f32 v6, v7, v8
	v_mul_f32_e32 v8, 0x43800000, v105
	v_mul_f32_e32 v11, 0x43800000, v109
	v_mov_b32_e32 v7, v143
	v_cvt_pk_fp8_f32 v7, v8, v11
	v_mul_f32_e32 v9, 0x43800000, v121
	v_mul_f32_e32 v10, 0x43800000, v125
	v_cvt_pk_fp8_f32 v6, v9, v10 op_sel:[0,0,1]
	v_mul_f32_e32 v8, 0x43800000, v81
	v_mul_f32_e32 v9, 0x43800000, v85
	v_cvt_pk_fp8_f32 v7, v8, v9 op_sel:[0,0,1]
	v_mul_f32_e32 v9, 0x43800000, v90
	v_mul_f32_e32 v10, 0x43800000, v94
	v_mov_b32_e32 v8, v143
	v_cvt_pk_fp8_f32 v8, v9, v10
	v_mul_f32_e32 v10, 0x43800000, v114
	v_mul_f32_e32 v13, 0x43800000, v118
	v_mov_b32_e32 v9, v143
	v_cvt_pk_fp8_f32 v9, v10, v13
	v_mul_f32_e32 v11, 0x43800000, v130
	v_mul_f32_e32 v12, 0x43800000, v134
	v_cvt_pk_fp8_f32 v8, v11, v12 op_sel:[0,0,1]
	v_mul_f32_e32 v10, 0x43800000, v98
	v_mul_f32_e32 v11, 0x43800000, v102
	v_cvt_pk_fp8_f32 v9, v10, v11 op_sel:[0,0,1]
	v_mul_f32_e32 v11, 0x43800000, v74
	v_mul_f32_e32 v12, 0x43800000, v78
	v_mov_b32_e32 v10, v143
	v_cvt_pk_fp8_f32 v10, v11, v12
	v_mul_f32_e32 v12, 0x43800000, v106
	v_mul_f32_e32 v15, 0x43800000, v110
	v_mov_b32_e32 v11, v143
	v_cvt_pk_fp8_f32 v11, v12, v15
	v_mul_f32_e32 v13, 0x43800000, v122
	v_mul_f32_e32 v14, 0x43800000, v126
	v_cvt_pk_fp8_f32 v10, v13, v14 op_sel:[0,0,1]
	v_mul_f32_e32 v12, 0x43800000, v82
	v_mul_f32_e32 v13, 0x43800000, v86
	v_cvt_pk_fp8_f32 v11, v12, v13 op_sel:[0,0,1]
	v_mul_f32_e32 v13, 0x43800000, v91
	v_mul_f32_e32 v14, 0x43800000, v95
	v_mov_b32_e32 v12, v143
	v_cvt_pk_fp8_f32 v12, v13, v14
	v_mul_f32_e32 v14, 0x43800000, v115
	v_mul_f32_e32 v17, 0x43800000, v119
	v_mov_b32_e32 v13, v143
	v_cvt_pk_fp8_f32 v13, v14, v17
	v_mul_f32_e32 v15, 0x43800000, v131
	v_mul_f32_e32 v16, 0x43800000, v135
	v_cvt_pk_fp8_f32 v12, v15, v16 op_sel:[0,0,1]
	v_mul_f32_e32 v14, 0x43800000, v99
	v_mul_f32_e32 v15, 0x43800000, v103
	v_cvt_pk_fp8_f32 v13, v14, v15 op_sel:[0,0,1]
	v_mul_f32_e32 v15, 0x43800000, v75
	v_mul_f32_e32 v16, 0x43800000, v79
	v_mov_b32_e32 v14, v143
	v_cvt_pk_fp8_f32 v14, v15, v16
	v_mul_f32_e32 v16, 0x43800000, v107
	v_mul_f32_e32 v19, 0x43800000, v111
	v_mov_b32_e32 v15, v143
	v_cvt_pk_fp8_f32 v15, v16, v19
	v_mul_f32_e32 v17, 0x43800000, v123
	v_mul_f32_e32 v18, 0x43800000, v127
	v_cvt_pk_fp8_f32 v14, v17, v18 op_sel:[0,0,1]
	v_mul_f32_e32 v16, 0x43800000, v83
	v_mul_f32_e32 v17, 0x43800000, v87
	v_cvt_pk_fp8_f32 v15, v16, v17 op_sel:[0,0,1]
	ds_write_b128 v194, v[0:3] offset:32
	ds_write_b128 v194, v[4:7] offset:2592
	ds_write_b128 v194, v[8:11] offset:5152
	ds_write_b128 v194, v[12:15] offset:7712
	s_waitcnt lgkmcnt(0)
	ds_read_b128 v[0:3], v195
	v_add_u32_e32 v4, s6, v181
	v_ashrrev_i32_e32 v5, 31, v4
	v_lshl_add_u64 v[8:9], s[68:69], 0, v[144:145]
	v_lshlrev_b64 v[4:5], 10, v[4:5]
	v_lshl_add_u64 v[10:11], v[8:9], 0, v[4:5]
	ds_read_b128 v[4:7], v195 offset:1280
	s_waitcnt lgkmcnt(1)
	global_store_dwordx4 v[10:11], v[0:3], off
	s_nop 1
	v_add_u32_e32 v0, s6, v182
	v_ashrrev_i32_e32 v1, 31, v0
	v_lshlrev_b64 v[0:1], 10, v[0:1]
	v_lshl_add_u64 v[0:1], v[8:9], 0, v[0:1]
	s_waitcnt lgkmcnt(0)
	global_store_dwordx4 v[0:1], v[4:7], off
	ds_read_b128 v[0:3], v195 offset:2560
	s_nop 0
	v_add_u32_e32 v4, s6, v183
	v_ashrrev_i32_e32 v5, 31, v4
	v_lshlrev_b64 v[4:5], 10, v[4:5]
	v_lshl_add_u64 v[10:11], v[8:9], 0, v[4:5]
	ds_read_b128 v[4:7], v195 offset:3840
	s_waitcnt lgkmcnt(1)
	global_store_dwordx4 v[10:11], v[0:3], off
	s_nop 1
	v_add_u32_e32 v0, s6, v184
	v_ashrrev_i32_e32 v1, 31, v0
	v_lshlrev_b64 v[0:1], 10, v[0:1]
	v_lshl_add_u64 v[0:1], v[8:9], 0, v[0:1]
	s_waitcnt lgkmcnt(0)
	global_store_dwordx4 v[0:1], v[4:7], off
	ds_read_b128 v[0:3], v195 offset:5120
	s_nop 0
	v_add_u32_e32 v4, s6, v185
	v_ashrrev_i32_e32 v5, 31, v4
	v_lshlrev_b64 v[4:5], 10, v[4:5]
	v_lshl_add_u64 v[10:11], v[8:9], 0, v[4:5]
	ds_read_b128 v[4:7], v195 offset:6400
	s_waitcnt lgkmcnt(1)
	global_store_dwordx4 v[10:11], v[0:3], off
	s_nop 1
	v_add_u32_e32 v0, s6, v186
	v_ashrrev_i32_e32 v1, 31, v0
	v_lshlrev_b64 v[0:1], 10, v[0:1]
	v_lshl_add_u64 v[0:1], v[8:9], 0, v[0:1]
	s_waitcnt lgkmcnt(0)
	global_store_dwordx4 v[0:1], v[4:7], off
	ds_read_b128 v[0:3], v195 offset:7680
	s_nop 0
	v_add_u32_e32 v4, s6, v187
	v_ashrrev_i32_e32 v5, 31, v4
	v_lshlrev_b64 v[4:5], 10, v[4:5]
	v_lshl_add_u64 v[10:11], v[8:9], 0, v[4:5]
	ds_read_b128 v[4:7], v195 offset:8960
	s_waitcnt lgkmcnt(1)
	global_store_dwordx4 v[10:11], v[0:3], off
	s_nop 1
	v_add_u32_e32 v0, s6, v188
	v_ashrrev_i32_e32 v1, 31, v0
	v_lshlrev_b64 v[0:1], 10, v[0:1]
	v_lshl_add_u64 v[0:1], v[8:9], 0, v[0:1]
	s_waitcnt lgkmcnt(0)
	global_store_dwordx4 v[0:1], v[4:7], off
	s_waitcnt lgkmcnt(0)
	s_mov_b64 s[6:7], 0
; #define LAS __attribute__((address_space(3)))
; __device__ __forceinline__ unsigned pk4_fp8(float x0, float x1, float x2, float x3) { int w = 0; w = __builtin_amdgcn_cvt_pk_fp8_f32(x0, x1, w, false); w = __builtin_amdgcn_cvt_pk_fp8_f32(x2, x3, w, true); return (unsigned)w; }
; __device__ __forceinline__ void transpose_item_fp8w(const float* W, int K, int N, unsigned char* WT, float q, LAS unsigned char* scr, int item, int lane) {
;     const int nblk = N / 128, kb = item / nblk, nb = item % nblk, k0 = 64 * kb, n0 = 128 * nb;
;     const int l5 = lane & 31, h = lane >> 5;
;     const float* src = W + (size_t)(k0 + 16 * h) * N + n0 + 4 * l5;
; #pragma unroll
;     for (int b = 0; b < 2; ++b) {
;         f32x4 x[16];
; #pragma unroll
;         for (int s_ = 0; s_ < 16; ++s_) x[s_] = *(const f32x4*)(src + (size_t)(32 * b + s_) * N);
; #pragma unroll
;         for (int i = 0; i < 4; ++i) {
;             u32x4 o;
;             o.x = pk4_fp8(x[0][i] * q, x[1][i] * q, x[2][i] * q, x[3][i] * q); o.y = pk4_fp8(x[4][i] * q, x[5][i] * q, x[6][i] * q, x[7][i] * q);
;             o.z = pk4_fp8(x[8][i] * q, x[9][i] * q, x[10][i] * q, x[11][i] * q); o.w = pk4_fp8(x[12][i] * q, x[13][i] * q, x[14][i] * q, x[15][i] * q);
;             *(LAS u32x4*)(scr + (l5 + 32 * i) * 80 + (2 * b + h) * 16) = o; }
.LBB0_44:
	s_andn2_b64 vcc, exec, s[6:7]
	s_cbranch_vccnz .LBB0_46
	s_add_i32 s67, s66, 0xfffff910
	s_lshr_b32 s4, s67, 8
	s_lshl_b64 s[6:7], s[4:5], 23
	s_add_u32 s68, s18, s6
	s_addc_u32 s69, s19, s7
	s_lshl_b64 s[8:9], s[4:5], 21
	v_readlane_b32 s4, v246, 15
	s_add_u32 s7, s4, s8
	v_readlane_b32 s4, v246, 16
	s_addc_u32 s8, s4, s9
	s_lshl_b32 s4, s67, 6
	s_and_b32 s9, s4, 0x3c0
	v_add_u32_e32 v0, s9, v177
	s_lshl_b32 s4, s67, 3
	v_ashrrev_i32_e32 v1, 31, v0
	s_and_b32 s6, s4, 0x780
	v_lshlrev_b64 v[0:1], 13, v[0:1]
	v_lshl_add_u64 v[0:1], s[68:69], 0, v[0:1]
	s_lshl_b32 s4, s6, 2
	v_lshl_add_u64 v[0:1], v[0:1], 0, s[4:5]
	v_lshl_add_u64 v[128:129], v[0:1], 0, v[142:143]
	v_add_co_u32_e32 v4, vcc, s10, v128
	v_mov_b32_e32 v64, v143
	s_nop 0
	v_addc_co_u32_e32 v5, vcc, 0, v129, vcc
	v_add_co_u32_e32 v8, vcc, s11, v128
	global_load_dwordx4 v[0:3], v[128:129], off
	s_nop 0
	global_load_dwordx4 v[4:7], v[4:5], off
	v_addc_co_u32_e32 v9, vcc, 0, v129, vcc
	v_add_co_u32_e32 v12, vcc, s15, v128
	v_mov_b32_e32 v65, v143
	s_nop 0
	v_addc_co_u32_e32 v13, vcc, 0, v129, vcc
	v_add_co_u32_e32 v16, vcc, s20, v128
	global_load_dwordx4 v[8:11], v[8:9], off
	s_nop 0
	global_load_dwordx4 v[12:15], v[12:13], off
	v_addc_co_u32_e32 v17, vcc, 0, v129, vcc
	v_add_co_u32_e32 v20, vcc, s21, v128
	v_mov_b32_e32 v66, v143
	s_nop 0
	v_addc_co_u32_e32 v21, vcc, 0, v129, vcc
	v_add_co_u32_e32 v24, vcc, s22, v128
	global_load_dwordx4 v[16:19], v[16:17], off
	s_nop 0
	global_load_dwordx4 v[20:23], v[20:21], off
	v_addc_co_u32_e32 v25, vcc, 0, v129, vcc
	v_add_co_u32_e32 v28, vcc, s23, v128
	v_mov_b32_e32 v67, v143
	s_nop 0
	v_addc_co_u32_e32 v29, vcc, 0, v129, vcc
	v_add_co_u32_e32 v32, vcc, s34, v128
	global_load_dwordx4 v[24:27], v[24:25], off
	s_nop 0
	global_load_dwordx4 v[28:31], v[28:29], off
	v_addc_co_u32_e32 v33, vcc, 0, v129, vcc
	v_add_co_u32_e32 v36, vcc, s35, v128
	v_mov_b32_e32 v96, v143
	s_nop 0
	v_addc_co_u32_e32 v37, vcc, 0, v129, vcc
	v_add_co_u32_e32 v40, vcc, s36, v128
	global_load_dwordx4 v[32:35], v[32:33], off
	s_nop 0
	global_load_dwordx4 v[36:39], v[36:37], off
	v_addc_co_u32_e32 v41, vcc, 0, v129, vcc
	v_add_co_u32_e32 v44, vcc, s37, v128
	v_mov_b32_e32 v97, v143
	s_nop 0
	v_addc_co_u32_e32 v45, vcc, 0, v129, vcc
	v_add_co_u32_e32 v48, vcc, s38, v128
	global_load_dwordx4 v[40:43], v[40:41], off
	s_nop 0
	global_load_dwordx4 v[44:47], v[44:45], off
	v_addc_co_u32_e32 v49, vcc, 0, v129, vcc
	v_add_co_u32_e32 v52, vcc, s39, v128
	v_mov_b32_e32 v98, v143
	s_nop 0
	v_addc_co_u32_e32 v53, vcc, 0, v129, vcc
	global_load_dwordx4 v[48:51], v[48:49], off
	s_nop 0
	global_load_dwordx4 v[52:55], v[52:53], off
	v_add_co_u32_e32 v56, vcc, s40, v128
	v_mov_b32_e32 v99, v143
	s_nop 0
	v_addc_co_u32_e32 v57, vcc, 0, v129, vcc
	v_add_co_u32_e32 v60, vcc, s41, v128
	v_mov_b32_e32 v136, v143
	s_nop 0
	v_addc_co_u32_e32 v61, vcc, 0, v129, vcc
	global_load_dwordx4 v[56:59], v[56:57], off
	s_nop 0
	global_load_dwordx4 v[60:63], v[60:61], off
	v_mov_b32_e32 v137, v143
	v_mov_b32_e32 v138, v143
	v_mov_b32_e32 v139, v143
	s_add_u32 s68, s7, s9
	s_addc_u32 s69, s8, 0
	s_waitcnt vmcnt(15)
	v_mul_f32_e32 v0, 0x43000000, v0
	s_waitcnt vmcnt(14)
	v_mul_f32_e32 v4, 0x43000000, v4
	v_cvt_pk_fp8_f32 v64, v0, v4
	s_waitcnt vmcnt(13)
	v_mul_f32_e32 v8, 0x43000000, v8
	s_waitcnt vmcnt(12)
	v_mul_f32_e32 v12, 0x43000000, v12
	v_cvt_pk_fp8_f32 v64, v8, v12 op_sel:[0,0,1]
	s_waitcnt vmcnt(11)
	v_mul_f32_e32 v0, 0x43000000, v16
	s_waitcnt vmcnt(10)
	v_mul_f32_e32 v4, 0x43000000, v20
	v_cvt_pk_fp8_f32 v65, v0, v4
	s_waitcnt vmcnt(9)
	v_mul_f32_e32 v0, 0x43000000, v24
	s_waitcnt vmcnt(8)
	v_mul_f32_e32 v4, 0x43000000, v28
	v_cvt_pk_fp8_f32 v65, v0, v4 op_sel:[0,0,1]
	s_waitcnt vmcnt(7)
	v_mul_f32_e32 v0, 0x43000000, v32
	s_waitcnt vmcnt(6)
	v_mul_f32_e32 v4, 0x43000000, v36
	v_cvt_pk_fp8_f32 v66, v0, v4
	s_waitcnt vmcnt(5)
	v_mul_f32_e32 v8, 0x43000000, v40
	s_waitcnt vmcnt(4)
	v_mul_f32_e32 v12, 0x43000000, v44
	v_cvt_pk_fp8_f32 v66, v8, v12 op_sel:[0,0,1]
	v_mul_f32_e32 v8, 0x43000000, v18
	s_waitcnt vmcnt(3)
	v_mul_f32_e32 v0, 0x43000000, v48
	s_waitcnt vmcnt(2)
	v_mul_f32_e32 v4, 0x43000000, v52
	v_cvt_pk_fp8_f32 v67, v0, v4
	s_waitcnt vmcnt(1)
	v_mul_f32_e32 v0, 0x43000000, v56
	s_waitcnt vmcnt(0)
	v_mul_f32_e32 v4, 0x43000000, v60
	v_cvt_pk_fp8_f32 v67, v0, v4 op_sel:[0,0,1]
	v_mul_f32_e32 v0, 0x43000000, v1
	v_mul_f32_e32 v1, 0x43000000, v5
	v_cvt_pk_fp8_f32 v96, v0, v1
	v_mul_f32_e32 v0, 0x43000000, v17
	v_mul_f32_e32 v1, 0x43000000, v21
	v_cvt_pk_fp8_f32 v97, v0, v1
	v_mul_f32_e32 v0, 0x43000000, v25
	v_mul_f32_e32 v1, 0x43000000, v29
	v_mul_f32_e32 v4, 0x43000000, v9
	v_cvt_pk_fp8_f32 v97, v0, v1 op_sel:[0,0,1]
	v_mul_f32_e32 v0, 0x43000000, v33
	v_mul_f32_e32 v1, 0x43000000, v37
	v_cvt_pk_fp8_f32 v98, v0, v1
	v_mul_f32_e32 v0, 0x43000000, v49
	v_mul_f32_e32 v1, 0x43000000, v53
	v_cvt_pk_fp8_f32 v99, v0, v1
	v_mul_f32_e32 v0, 0x43000000, v57
	v_mul_f32_e32 v1, 0x43000000, v61
	v_mul_f32_e32 v5, 0x43000000, v13
	v_cvt_pk_fp8_f32 v99, v0, v1 op_sel:[0,0,1]
	v_mul_f32_e32 v0, 0x43000000, v2
	v_mul_f32_e32 v1, 0x43000000, v6
	v_cvt_pk_fp8_f32 v136, v0, v1
	v_add_co_u32_e32 v0, vcc, s42, v128
	v_cvt_pk_fp8_f32 v96, v4, v5 op_sel:[0,0,1]
	v_mul_f32_e32 v4, 0x43000000, v41
	v_mul_f32_e32 v5, 0x43000000, v45
	v_addc_co_u32_e32 v1, vcc, 0, v129, vcc
	v_cvt_pk_fp8_f32 v98, v4, v5 op_sel:[0,0,1]
	v_add_co_u32_e32 v4, vcc, s43, v128
	v_mul_f32_e32 v2, 0x43000000, v10
	s_nop 0
	v_addc_co_u32_e32 v5, vcc, 0, v129, vcc
	global_load_dwordx4 v[68:71], v[0:1], off
	global_load_dwordx4 v[72:75], v[4:5], off
	v_add_co_u32_e32 v0, vcc, s44, v128
	v_mul_f32_e32 v6, 0x43000000, v14
	s_nop 0
	v_addc_co_u32_e32 v1, vcc, 0, v129, vcc
	v_add_co_u32_e32 v4, vcc, s45, v128
	v_cvt_pk_fp8_f32 v136, v2, v6 op_sel:[0,0,1]
	s_nop 0
	v_addc_co_u32_e32 v5, vcc, 0, v129, vcc
	global_load_dwordx4 v[76:79], v[0:1], off
	global_load_dwordx4 v[80:83], v[4:5], off
	v_add_co_u32_e32 v0, vcc, s46, v128
	v_mul_f32_e32 v2, 0x43000000, v42
	s_nop 0
	v_addc_co_u32_e32 v1, vcc, 0, v129, vcc
	v_add_co_u32_e32 v4, vcc, s47, v128
	v_mul_f32_e32 v6, 0x43000000, v47
	s_nop 0
	v_addc_co_u32_e32 v5, vcc, 0, v129, vcc
	global_load_dwordx4 v[84:87], v[0:1], off
	global_load_dwordx4 v[88:91], v[4:5], off
	v_add_co_u32_e32 v0, vcc, s48, v128
	s_waitcnt vmcnt(2)
; #define LAS __attribute__((address_space(3)))
; __device__ __forceinline__ unsigned pk4_fp8(float x0, float x1, float x2, float x3) { int w = 0; w = __builtin_amdgcn_cvt_pk_fp8_f32(x0, x1, w, false); w = __builtin_amdgcn_cvt_pk_fp8_f32(x2, x3, w, true); return (unsigned)w; }
; __device__ __forceinline__ void transpose_item_fp8w(const float* W, int K, int N, unsigned char* WT, float q, LAS unsigned char* scr, int item, int lane) {
;     ...
;     for (int b = 0; b < 2; ++b) {
;         f32x4 x[16];
; #pragma unroll
;         for (int s_ = 0; s_ < 16; ++s_) x[s_] = *(const f32x4*)(src + (size_t)(32 * b + s_) * N);
; #pragma unroll
;         for (int i = 0; i < 4; ++i) {
;             u32x4 o;
;             o.x = pk4_fp8(x[0][i] * q, x[1][i] * q, x[2][i] * q, x[3][i] * q); o.y = pk4_fp8(x[4][i] * q, x[5][i] * q, x[6][i] * q, x[7][i] * q);
;             o.z = pk4_fp8(x[8][i] * q, x[9][i] * q, x[10][i] * q, x[11][i] * q); o.w = pk4_fp8(x[12][i] * q, x[13][i] * q, x[14][i] * q, x[15][i] * q);
;             *(LAS u32x4*)(scr + (l5 + 32 * i) * 80 + (2 * b + h) * 16) = o; }
	v_mul_f32_e32 v12, 0x43000000, v82
	v_addc_co_u32_e32 v1, vcc, 0, v129, vcc
	v_add_co_u32_e32 v4, vcc, s49, v128
	v_mul_f32_e32 v16, 0x43000000, v83
	s_nop 0
	v_addc_co_u32_e32 v5, vcc, 0, v129, vcc
	global_load_dwordx4 v[92:95], v[0:1], off
	global_load_dwordx4 v[100:103], v[4:5], off
	v_add_co_u32_e32 v0, vcc, s50, v128
	s_waitcnt vmcnt(2)
	v_mul_f32_e32 v9, 0x43000000, v89
	v_addc_co_u32_e32 v1, vcc, 0, v129, vcc
	v_add_co_u32_e32 v4, vcc, s51, v128
	v_mul_f32_e32 v13, 0x43000000, v90
	s_nop 0
	v_addc_co_u32_e32 v5, vcc, 0, v129, vcc
	global_load_dwordx4 v[104:107], v[0:1], off
	global_load_dwordx4 v[108:111], v[4:5], off
	v_add_co_u32_e32 v0, vcc, s52, v128
	v_mul_f32_e32 v17, 0x43000000, v91
	s_nop 0
	v_addc_co_u32_e32 v1, vcc, 0, v129, vcc
	v_add_co_u32_e32 v4, vcc, s53, v128
	s_nop 1
	v_addc_co_u32_e32 v5, vcc, 0, v129, vcc
	global_load_dwordx4 v[112:115], v[0:1], off
	global_load_dwordx4 v[116:119], v[4:5], off
	v_add_co_u32_e32 v0, vcc, s54, v128
	s_waitcnt vmcnt(0)
	v_mul_f32_e32 v10, 0x43000000, v117
	v_addc_co_u32_e32 v1, vcc, 0, v129, vcc
	v_add_co_u32_e32 v4, vcc, s55, v128
	v_mul_f32_e32 v14, 0x43000000, v118
	s_nop 0
	v_addc_co_u32_e32 v5, vcc, 0, v129, vcc
	global_load_dwordx4 v[120:123], v[0:1], off
	global_load_dwordx4 v[124:127], v[4:5], off
	v_add_co_u32_e32 v0, vcc, s56, v128
	v_mul_f32_e32 v18, 0x43000000, v119
	s_nop 0
	v_addc_co_u32_e32 v1, vcc, 0, v129, vcc
	v_add_co_u32_e32 v4, vcc, s57, v128
	s_nop 1
	v_addc_co_u32_e32 v5, vcc, 0, v129, vcc
	global_load_dwordx4 v[128:131], v[0:1], off
	global_load_dwordx4 v[132:135], v[4:5], off
	v_mul_f32_e32 v0, 0x43000000, v22
	v_cvt_pk_fp8_f32 v137, v8, v0
	v_mul_f32_e32 v0, 0x43000000, v26
	v_mul_f32_e32 v1, 0x43000000, v30
	v_mul_f32_e32 v4, 0x43000000, v46
	v_cvt_pk_fp8_f32 v137, v0, v1 op_sel:[0,0,1]
	v_mul_f32_e32 v0, 0x43000000, v34
	v_mul_f32_e32 v1, 0x43000000, v38
	v_cvt_pk_fp8_f32 v138, v0, v1
	v_mul_f32_e32 v0, 0x43000000, v50
	v_mul_f32_e32 v1, 0x43000000, v54
	v_cvt_pk_fp8_f32 v139, v0, v1
	v_mul_f32_e32 v0, 0x43000000, v58
	v_mul_f32_e32 v1, 0x43000000, v62
	v_cvt_pk_fp8_f32 v138, v2, v4 op_sel:[0,0,1]
	v_cvt_pk_fp8_f32 v139, v0, v1 op_sel:[0,0,1]
	v_mul_f32_e32 v1, 0x43000000, v3
	v_mul_f32_e32 v2, 0x43000000, v7
	v_mov_b32_e32 v0, v143
	v_cvt_pk_fp8_f32 v0, v1, v2
	v_mul_f32_e32 v2, 0x43000000, v19
	v_mul_f32_e32 v5, 0x43000000, v23
	v_mov_b32_e32 v1, v143
	v_cvt_pk_fp8_f32 v1, v2, v5
	v_mul_f32_e32 v3, 0x43000000, v11
	v_mul_f32_e32 v4, 0x43000000, v15
	v_cvt_pk_fp8_f32 v0, v3, v4 op_sel:[0,0,1]
	v_mul_f32_e32 v2, 0x43000000, v27
	v_mul_f32_e32 v3, 0x43000000, v31
	v_cvt_pk_fp8_f32 v1, v2, v3 op_sel:[0,0,1]
	v_mul_f32_e32 v3, 0x43000000, v35
	v_mul_f32_e32 v4, 0x43000000, v39
	v_mov_b32_e32 v2, v143
	v_cvt_pk_fp8_f32 v2, v3, v4
	v_mul_f32_e32 v4, 0x43000000, v51
	v_mul_f32_e32 v7, 0x43000000, v55
	v_mov_b32_e32 v3, v143
	v_cvt_pk_fp8_f32 v3, v4, v7
	v_mul_f32_e32 v5, 0x43000000, v43
	v_cvt_pk_fp8_f32 v2, v5, v6 op_sel:[0,0,1]
	v_mul_f32_e32 v4, 0x43000000, v59
	v_mul_f32_e32 v5, 0x43000000, v63
	v_cvt_pk_fp8_f32 v3, v4, v5 op_sel:[0,0,1]
	ds_write_b128 v194, v[64:67]
	ds_write_b128 v194, v[96:99] offset:2560
	ds_write_b128 v194, v[136:139] offset:5120
	ds_write_b128 v194, v[0:3] offset:7680
	v_mul_f32_e32 v1, 0x43000000, v68
	v_mul_f32_e32 v2, 0x43000000, v72
	v_mov_b32_e32 v0, v143
	v_cvt_pk_fp8_f32 v0, v1, v2
	v_mul_f32_e32 v2, 0x43000000, v84
	v_mul_f32_e32 v5, 0x43000000, v88
	v_mov_b32_e32 v1, v143
	v_cvt_pk_fp8_f32 v1, v2, v5
	v_mul_f32_e32 v3, 0x43000000, v76
	v_mul_f32_e32 v4, 0x43000000, v80
	v_cvt_pk_fp8_f32 v0, v3, v4 op_sel:[0,0,1]
	v_mul_f32_e32 v2, 0x43000000, v92
	v_mul_f32_e32 v3, 0x43000000, v100
	v_cvt_pk_fp8_f32 v1, v2, v3 op_sel:[0,0,1]
	v_mul_f32_e32 v3, 0x43000000, v104
	v_mul_f32_e32 v4, 0x43000000, v108
	v_mov_b32_e32 v2, v143
	v_cvt_pk_fp8_f32 v2, v3, v4
	v_mov_b32_e32 v3, v143
	v_mul_f32_e32 v5, 0x43000000, v112
	v_mul_f32_e32 v6, 0x43000000, v116
	v_cvt_pk_fp8_f32 v2, v5, v6 op_sel:[0,0,1]
	v_mul_f32_e32 v6, 0x43000000, v73
	s_waitcnt vmcnt(3)
	v_mul_f32_e32 v4, 0x43000000, v120
	s_waitcnt vmcnt(2)
	v_mul_f32_e32 v7, 0x43000000, v124
	v_cvt_pk_fp8_f32 v3, v4, v7
	v_mul_f32_e32 v7, 0x43000000, v77
	v_mul_f32_e32 v8, 0x43000000, v81
	v_mul_f32_e32 v11, 0x43000000, v125
	v_mul_f32_e32 v15, 0x43000000, v126
	v_mul_f32_e32 v19, 0x43000000, v127
	s_waitcnt vmcnt(1)
	v_mul_f32_e32 v4, 0x43000000, v128
	s_waitcnt vmcnt(0)
; #define LAS __attribute__((address_space(3)))
; __device__ __forceinline__ unsigned pk4_fp8(float x0, float x1, float x2, float x3) { int w = 0; w = __builtin_amdgcn_cvt_pk_fp8_f32(x0, x1, w, false); w = __builtin_amdgcn_cvt_pk_fp8_f32(x2, x3, w, true); return (unsigned)w; }
; __device__ __forceinline__ void transpose_item_fp8w(const float* W, int K, int N, unsigned char* WT, float q, LAS unsigned char* scr, int item, int lane) {
;     ...
; #pragma unroll
;         for (int i = 0; i < 4; ++i) {
;             u32x4 o;
;             o.x = pk4_fp8(x[0][i] * q, x[1][i] * q, x[2][i] * q, x[3][i] * q); o.y = pk4_fp8(x[4][i] * q, x[5][i] * q, x[6][i] * q, x[7][i] * q);
;             o.z = pk4_fp8(x[8][i] * q, x[9][i] * q, x[10][i] * q, x[11][i] * q); o.w = pk4_fp8(x[12][i] * q, x[13][i] * q, x[14][i] * q, x[15][i] * q);
;             *(LAS u32x4*)(scr + (l5 + 32 * i) * 80 + (2 * b + h) * 16) = o; }
;     }
;     asm volatile("s_waitcnt lgkmcnt(0)" ::: "memory");
; #pragma unroll
;     for (int qd = 0; qd < 8; ++qd) {
;         const int rho = 16 * qd + (lane >> 2), piece = lane & 3;
;         const u32x4 o = *(const LAS u32x4*)(scr + rho * 80 + piece * 16);
;         const int nl = 4 * (rho & 31) + (rho >> 5);
;         *(u32x4*)(WT + (size_t)(n0 + nl) * K + k0 + piece * 16) = o; }
;     asm volatile("s_waitcnt lgkmcnt(0)" ::: "memory");
	v_mul_f32_e32 v5, 0x43000000, v132
	v_cvt_pk_fp8_f32 v3, v4, v5 op_sel:[0,0,1]
	v_mul_f32_e32 v5, 0x43000000, v69
	v_mov_b32_e32 v4, v143
	v_cvt_pk_fp8_f32 v4, v5, v6
	v_mul_f32_e32 v6, 0x43000000, v85
	v_mov_b32_e32 v5, v143
	v_cvt_pk_fp8_f32 v5, v6, v9
	v_cvt_pk_fp8_f32 v4, v7, v8 op_sel:[0,0,1]
	v_mul_f32_e32 v6, 0x43000000, v93
	v_mul_f32_e32 v7, 0x43000000, v101
	v_cvt_pk_fp8_f32 v5, v6, v7 op_sel:[0,0,1]
	v_mul_f32_e32 v7, 0x43000000, v105
	v_mul_f32_e32 v8, 0x43000000, v109
	v_mov_b32_e32 v6, v143
	v_cvt_pk_fp8_f32 v6, v7, v8
	v_mul_f32_e32 v8, 0x43000000, v121
	v_mov_b32_e32 v7, v143
	v_cvt_pk_fp8_f32 v7, v8, v11
	v_mul_f32_e32 v9, 0x43000000, v113
	v_cvt_pk_fp8_f32 v6, v9, v10 op_sel:[0,0,1]
	v_mul_f32_e32 v8, 0x43000000, v129
	v_mul_f32_e32 v9, 0x43000000, v133
	v_cvt_pk_fp8_f32 v7, v8, v9 op_sel:[0,0,1]
	v_mul_f32_e32 v9, 0x43000000, v70
	v_mul_f32_e32 v10, 0x43000000, v74
	v_mov_b32_e32 v8, v143
	v_cvt_pk_fp8_f32 v8, v9, v10
	v_mul_f32_e32 v10, 0x43000000, v86
	v_mov_b32_e32 v9, v143
	v_cvt_pk_fp8_f32 v9, v10, v13
	v_mul_f32_e32 v11, 0x43000000, v78
	v_cvt_pk_fp8_f32 v8, v11, v12 op_sel:[0,0,1]
	v_mul_f32_e32 v10, 0x43000000, v94
	v_mul_f32_e32 v11, 0x43000000, v102
	v_cvt_pk_fp8_f32 v9, v10, v11 op_sel:[0,0,1]
	v_mul_f32_e32 v11, 0x43000000, v106
	v_mul_f32_e32 v12, 0x43000000, v110
	v_mov_b32_e32 v10, v143
	v_cvt_pk_fp8_f32 v10, v11, v12
	v_mul_f32_e32 v12, 0x43000000, v122
	v_mov_b32_e32 v11, v143
	v_cvt_pk_fp8_f32 v11, v12, v15
	v_mul_f32_e32 v13, 0x43000000, v114
	v_cvt_pk_fp8_f32 v10, v13, v14 op_sel:[0,0,1]
	v_mul_f32_e32 v12, 0x43000000, v130
	v_mul_f32_e32 v13, 0x43000000, v134
	v_cvt_pk_fp8_f32 v11, v12, v13 op_sel:[0,0,1]
	v_mul_f32_e32 v13, 0x43000000, v71
	v_mul_f32_e32 v14, 0x43000000, v75
	v_mov_b32_e32 v12, v143
	v_cvt_pk_fp8_f32 v12, v13, v14
	v_mul_f32_e32 v14, 0x43000000, v87
	v_mov_b32_e32 v13, v143
	v_cvt_pk_fp8_f32 v13, v14, v17
	v_mul_f32_e32 v15, 0x43000000, v79
	v_cvt_pk_fp8_f32 v12, v15, v16 op_sel:[0,0,1]
	v_mul_f32_e32 v14, 0x43000000, v95
	v_mul_f32_e32 v15, 0x43000000, v103
	v_cvt_pk_fp8_f32 v13, v14, v15 op_sel:[0,0,1]
	v_mul_f32_e32 v15, 0x43000000, v107
	v_mul_f32_e32 v16, 0x43000000, v111
	v_mov_b32_e32 v14, v143
	v_cvt_pk_fp8_f32 v14, v15, v16
	v_mul_f32_e32 v16, 0x43000000, v123
	v_mov_b32_e32 v15, v143
	v_cvt_pk_fp8_f32 v15, v16, v19
	v_mul_f32_e32 v17, 0x43000000, v115
	v_cvt_pk_fp8_f32 v14, v17, v18 op_sel:[0,0,1]
	v_mul_f32_e32 v16, 0x43000000, v131
	v_mul_f32_e32 v17, 0x43000000, v135
	v_cvt_pk_fp8_f32 v15, v16, v17 op_sel:[0,0,1]
	ds_write_b128 v194, v[0:3] offset:32
	ds_write_b128 v194, v[4:7] offset:2592
	ds_write_b128 v194, v[8:11] offset:5152
	ds_write_b128 v194, v[12:15] offset:7712
	s_waitcnt lgkmcnt(0)
	ds_read_b128 v[0:3], v195
	v_add_u32_e32 v4, s6, v181
	v_ashrrev_i32_e32 v5, 31, v4
	v_lshl_add_u64 v[8:9], s[68:69], 0, v[144:145]
	v_lshlrev_b64 v[4:5], 10, v[4:5]
	v_lshl_add_u64 v[10:11], v[8:9], 0, v[4:5]
	ds_read_b128 v[4:7], v195 offset:1280
	s_waitcnt lgkmcnt(1)
	global_store_dwordx4 v[10:11], v[0:3], off
	s_nop 1
	v_add_u32_e32 v0, s6, v182
	v_ashrrev_i32_e32 v1, 31, v0
	v_lshlrev_b64 v[0:1], 10, v[0:1]
	v_lshl_add_u64 v[0:1], v[8:9], 0, v[0:1]
	s_waitcnt lgkmcnt(0)
	global_store_dwordx4 v[0:1], v[4:7], off
	ds_read_b128 v[0:3], v195 offset:2560
	s_nop 0
	v_add_u32_e32 v4, s6, v183
	v_ashrrev_i32_e32 v5, 31, v4
	v_lshlrev_b64 v[4:5], 10, v[4:5]
	v_lshl_add_u64 v[10:11], v[8:9], 0, v[4:5]
	ds_read_b128 v[4:7], v195 offset:3840
	s_waitcnt lgkmcnt(1)
	global_store_dwordx4 v[10:11], v[0:3], off
	s_nop 1
	v_add_u32_e32 v0, s6, v184
	v_ashrrev_i32_e32 v1, 31, v0
	v_lshlrev_b64 v[0:1], 10, v[0:1]
	v_lshl_add_u64 v[0:1], v[8:9], 0, v[0:1]
	s_waitcnt lgkmcnt(0)
	global_store_dwordx4 v[0:1], v[4:7], off
	ds_read_b128 v[0:3], v195 offset:5120
	s_nop 0
	v_add_u32_e32 v4, s6, v185
	v_ashrrev_i32_e32 v5, 31, v4
	v_lshlrev_b64 v[4:5], 10, v[4:5]
	v_lshl_add_u64 v[10:11], v[8:9], 0, v[4:5]
	ds_read_b128 v[4:7], v195 offset:6400
	s_waitcnt lgkmcnt(1)
	global_store_dwordx4 v[10:11], v[0:3], off
	s_nop 1
	v_add_u32_e32 v0, s6, v186
	v_ashrrev_i32_e32 v1, 31, v0
	v_lshlrev_b64 v[0:1], 10, v[0:1]
	v_lshl_add_u64 v[0:1], v[8:9], 0, v[0:1]
	s_waitcnt lgkmcnt(0)
	global_store_dwordx4 v[0:1], v[4:7], off
	ds_read_b128 v[0:3], v195 offset:7680
	s_nop 0
	v_add_u32_e32 v4, s6, v187
	v_ashrrev_i32_e32 v5, 31, v4
	v_lshlrev_b64 v[4:5], 10, v[4:5]
	v_lshl_add_u64 v[10:11], v[8:9], 0, v[4:5]
	ds_read_b128 v[4:7], v195 offset:8960
	s_waitcnt lgkmcnt(1)
	global_store_dwordx4 v[10:11], v[0:3], off
	s_nop 1
	v_add_u32_e32 v0, s6, v188
	v_ashrrev_i32_e32 v1, 31, v0
	v_lshlrev_b64 v[0:1], 10, v[0:1]
	v_lshl_add_u64 v[0:1], v[8:9], 0, v[0:1]
	s_waitcnt lgkmcnt(0)
	global_store_dwordx4 v[0:1], v[4:7], off
	s_waitcnt lgkmcnt(0)

; #define LAS __attribute__((address_space(3)))
; __device__ __forceinline__ unsigned pk4_fp8(float x0, float x1, float x2, float x3) { int w = 0; w = __builtin_amdgcn_cvt_pk_fp8_f32(x0, x1, w, false); w = __builtin_amdgcn_cvt_pk_fp8_f32(x2, x3, w, true); return (unsigned)w; }
; __device__ __forceinline__ void transpose_item_fp8w(const float* W, int K, int N, unsigned char* WT, float q, LAS unsigned char* scr, int item, int lane) {
;     const int nblk = N / 128, kb = item / nblk, nb = item % nblk, k0 = 64 * kb, n0 = 128 * nb;
;     const int l5 = lane & 31, h = lane >> 5;
;     const float* src = W + (size_t)(k0 + 16 * h) * N + n0 + 4 * l5;
; #pragma unroll
;     for (int b = 0; b < 2; ++b) {
;         f32x4 x[16];
; #pragma unroll
;         for (int s_ = 0; s_ < 16; ++s_) x[s_] = *(const f32x4*)(src + (size_t)(32 * b + s_) * N);
; #pragma unroll
;         for (int i = 0; i < 4; ++i) {
;             u32x4 o;
;             o.x = pk4_fp8(x[0][i] * q, x[1][i] * q, x[2][i] * q, x[3][i] * q); o.y = pk4_fp8(x[4][i] * q, x[5][i] * q, x[6][i] * q, x[7][i] * q);
;             o.z = pk4_fp8(x[8][i] * q, x[9][i] * q, x[10][i] * q, x[11][i] * q); o.w = pk4_fp8(x[12][i] * q, x[13][i] * q, x[14][i] * q, x[15][i] * q);
;             *(LAS u32x4*)(scr + (l5 + 32 * i) * 80 + (2 * b + h) * 16) = o; }
.LBB0_331:
	s_cmpk_gt_i32 s5, 0x3df
	s_mov_b64 s[0:1], -1
	s_cbranch_scc0 .LBB0_359
	s_cmpk_gt_u32 s5, 0x46f
	s_cbranch_scc0 .LBB0_346
	s_cmpk_gt_u32 s5, 0x4ef
	s_cbranch_scc0 .LBB0_341
	s_cmpk_gt_u32 s5, 0x6ef
	s_cbranch_scc0 .LBB0_336
	s_add_i32 s2, s5, 0xfffff910
	v_readlane_b32 s8, v253, 32
	s_lshr_b32 s0, s2, 8
	v_readlane_b32 s9, v253, 33
	s_mov_b32 s13, s9
	s_add_i32 s12, s0, s21
	v_readlane_b32 s40, v253, 58
	s_lshl_b64 s[0:1], s[12:13], 23
	v_readlane_b32 s50, v254, 4
	v_readlane_b32 s51, v254, 5
	s_add_u32 s10, s50, s0
	s_addc_u32 s11, s51, s1
	s_lshl_b64 s[8:9], s[12:13], 21
	v_readlane_b32 s0, v246, 15
	s_add_u32 s1, s0, s8
	v_readlane_b32 s0, v246, 16
	s_addc_u32 s8, s0, s9
	s_lshl_b32 s0, s2, 6
	s_and_b32 s9, s0, 0x3c0
	v_add_u32_e32 v0, s9, v101
	s_lshl_b32 s0, s2, 3
	v_ashrrev_i32_e32 v1, 31, v0
	s_and_b32 s0, s0, 0x780
	v_lshlrev_b64 v[0:1], 13, v[0:1]
	v_lshl_add_u64 v[0:1], s[10:11], 0, v[0:1]
	s_lshl_b32 s12, s0, 2
	s_mov_b32 s3, s13
	v_readlane_b32 s41, v253, 59
	v_readlane_b32 s42, v253, 60
	v_readlane_b32 s43, v253, 61
	v_readlane_b32 s44, v253, 62
	v_readlane_b32 s45, v253, 63
	v_writelane_b32 v253, s2, 32
	v_lshl_add_u64 v[0:1], v[0:1], 0, s[12:13]
	v_lshl_add_u64 v[60:61], v[0:1], 0, v[152:153]
	v_writelane_b32 v253, s3, 33
	s_movk_i32 s2, 0x2000
	v_add_co_u32_e32 v4, vcc, s2, v60
	s_movk_i32 s2, 0x4000
	s_nop 0
	v_addc_co_u32_e32 v5, vcc, 0, v61, vcc
	v_add_co_u32_e32 v8, vcc, s2, v60
	s_movk_i32 s2, 0x6000
	s_nop 0
	v_addc_co_u32_e32 v9, vcc, 0, v61, vcc
	v_add_co_u32_e32 v12, vcc, s2, v60
	s_mov_b32 s2, 0x8000
	s_nop 0
	v_addc_co_u32_e32 v13, vcc, 0, v61, vcc
	v_add_co_u32_e32 v16, vcc, s2, v60
	s_mov_b32 s2, 0xa000
	s_nop 0
	v_addc_co_u32_e32 v17, vcc, 0, v61, vcc
	v_add_co_u32_e32 v20, vcc, s2, v60
	s_mov_b32 s2, 0xc000
	s_nop 0
	v_addc_co_u32_e32 v21, vcc, 0, v61, vcc
	v_add_co_u32_e32 v24, vcc, s2, v60
	s_mov_b32 s2, 0xe000
	s_nop 0
	v_addc_co_u32_e32 v25, vcc, 0, v61, vcc
	v_add_co_u32_e32 v28, vcc, s2, v60
	s_mov_b32 s2, 0x10000
	s_nop 0
	v_addc_co_u32_e32 v29, vcc, 0, v61, vcc
	v_add_co_u32_e32 v32, vcc, s2, v60
	s_mov_b32 s2, 0x12000
	s_nop 0
	v_addc_co_u32_e32 v33, vcc, 0, v61, vcc
	v_add_co_u32_e32 v36, vcc, s2, v60
	s_mov_b32 s2, 0x14000
	s_nop 0
	v_addc_co_u32_e32 v37, vcc, 0, v61, vcc
	v_add_co_u32_e32 v40, vcc, s2, v60
	s_mov_b32 s2, 0x16000
	s_nop 0
	v_addc_co_u32_e32 v41, vcc, 0, v61, vcc
	v_add_co_u32_e32 v44, vcc, s2, v60
	s_mov_b32 s2, 0x18000
	s_nop 0
	v_addc_co_u32_e32 v45, vcc, 0, v61, vcc
	v_add_co_u32_e32 v48, vcc, s2, v60
	global_load_dwordx4 v[0:3], v[60:61], off
	s_nop 0
	v_addc_co_u32_e32 v49, vcc, 0, v61, vcc
	global_load_dwordx4 v[4:7], v[4:5], off
	s_mov_b32 s2, 0x1a000
	global_load_dwordx4 v[12:15], v[12:13], off
	v_add_co_u32_e32 v52, vcc, s2, v60
	global_load_dwordx4 v[16:19], v[16:17], off
	s_nop 0
	v_addc_co_u32_e32 v53, vcc, 0, v61, vcc
	global_load_dwordx4 v[20:23], v[20:21], off
	s_mov_b32 s2, 0x1c000
	global_load_dwordx4 v[28:31], v[28:29], off
	v_add_co_u32_e32 v56, vcc, s2, v60
	global_load_dwordx4 v[32:35], v[32:33], off
	s_nop 0
	v_addc_co_u32_e32 v57, vcc, 0, v61, vcc
	global_load_dwordx4 v[36:39], v[36:37], off
	s_mov_b32 s2, 0x1e000
	global_load_dwordx4 v[44:47], v[44:45], off
	v_add_co_u32_e32 v62, vcc, s2, v60
	global_load_dwordx4 v[48:51], v[48:49], off
	s_nop 0
	v_addc_co_u32_e32 v63, vcc, 0, v61, vcc
	global_load_dwordx4 v[52:55], v[52:53], off
	v_mov_b32_e32 v120, v153
	global_load_dwordx4 v[8:11], v[8:9], off
	v_mov_b32_e32 v121, v153
	global_load_dwordx4 v[24:27], v[24:25], off
	v_mov_b32_e32 v122, v153
	global_load_dwordx4 v[40:43], v[40:41], off
	v_mov_b32_e32 v123, v153
	global_load_dwordx4 v[56:59], v[56:57], off
	s_mov_b32 s2, 0x40000
	global_load_dwordx4 v[116:119], v[62:63], off
	s_add_u32 s10, s1, s9
	s_addc_u32 s11, s8, 0
	v_readlane_b32 s46, v254, 0
	v_readlane_b32 s47, v254, 1
	v_readlane_b32 s48, v254, 2
	v_readlane_b32 s49, v254, 3
	v_readlane_b32 s52, v254, 6
	v_readlane_b32 s53, v254, 7
	v_readlane_b32 s54, v254, 8
	v_readlane_b32 s55, v254, 9
	s_waitcnt vmcnt(0)
	v_mul_f32_e32 v0, 0x43000000, v0
	s_waitcnt vmcnt(14)
	v_mul_f32_e32 v4, 0x43000000, v4
	v_cvt_pk_fp8_f32 v120, v0, v4
	s_waitcnt vmcnt(13)
	v_mul_f32_e32 v12, 0x43000000, v12
	s_waitcnt vmcnt(12)
	v_mul_f32_e32 v0, 0x43000000, v16
	s_waitcnt vmcnt(11)
	v_mul_f32_e32 v4, 0x43000000, v20
	v_cvt_pk_fp8_f32 v121, v0, v4
	s_waitcnt vmcnt(9)
	v_mul_f32_e32 v0, 0x43000000, v32
	s_waitcnt vmcnt(8)
	v_mul_f32_e32 v4, 0x43000000, v36
	v_cvt_pk_fp8_f32 v122, v0, v4
	s_waitcnt vmcnt(6)
	v_mul_f32_e32 v0, 0x43000000, v48
	s_waitcnt vmcnt(5)
	v_mul_f32_e32 v4, 0x43000000, v52
	v_cvt_pk_fp8_f32 v123, v0, v4
	s_waitcnt vmcnt(4)
	v_mul_f32_e32 v8, 0x43000000, v8
	v_cvt_pk_fp8_f32 v120, v8, v12 op_sel:[0,0,1]
	s_waitcnt vmcnt(3)
	v_mul_f32_e32 v8, 0x43000000, v24
	v_mul_f32_e32 v12, 0x43000000, v28
	v_cvt_pk_fp8_f32 v121, v8, v12 op_sel:[0,0,1]
	s_waitcnt vmcnt(2)
	v_mul_f32_e32 v8, 0x43000000, v40
	v_mul_f32_e32 v12, 0x43000000, v44
	v_cvt_pk_fp8_f32 v122, v8, v12 op_sel:[0,0,1]
	s_waitcnt vmcnt(1)
	v_mul_f32_e32 v8, 0x43000000, v56
	s_waitcnt vmcnt(0)
; #define LAS __attribute__((address_space(3)))
; __device__ __forceinline__ unsigned pk4_fp8(float x0, float x1, float x2, float x3) { int w = 0; w = __builtin_amdgcn_cvt_pk_fp8_f32(x0, x1, w, false); w = __builtin_amdgcn_cvt_pk_fp8_f32(x2, x3, w, true); return (unsigned)w; }
; __device__ __forceinline__ void transpose_item_fp8w(const float* W, int K, int N, unsigned char* WT, float q, LAS unsigned char* scr, int item, int lane) {
;     ...
;     for (int b = 0; b < 2; ++b) {
;         f32x4 x[16];
; #pragma unroll
;         for (int s_ = 0; s_ < 16; ++s_) x[s_] = *(const f32x4*)(src + (size_t)(32 * b + s_) * N);
; #pragma unroll
;         for (int i = 0; i < 4; ++i) {
;             u32x4 o;
;             o.x = pk4_fp8(x[0][i] * q, x[1][i] * q, x[2][i] * q, x[3][i] * q); o.y = pk4_fp8(x[4][i] * q, x[5][i] * q, x[6][i] * q, x[7][i] * q);
;             o.z = pk4_fp8(x[8][i] * q, x[9][i] * q, x[10][i] * q, x[11][i] * q); o.w = pk4_fp8(x[12][i] * q, x[13][i] * q, x[14][i] * q, x[15][i] * q);
;             *(LAS u32x4*)(scr + (l5 + 32 * i) * 80 + (2 * b + h) * 16) = o; }
;     }
;     asm volatile("s_waitcnt lgkmcnt(0)" ::: "memory");
; #pragma unroll
;     for (int qd = 0; qd < 8; ++qd) {
;         const int rho = 16 * qd + (lane >> 2), piece = lane & 3;
;         const u32x4 o = *(const LAS u32x4*)(scr + rho * 80 + piece * 16);
;         const int nl = 4 * (rho & 31) + (rho >> 5);
;         *(u32x4*)(WT + (size_t)(n0 + nl) * K + k0 + piece * 16) = o; }
	v_mul_f32_e32 v12, 0x43000000, v116
	v_cvt_pk_fp8_f32 v123, v8, v12 op_sel:[0,0,1]
	v_mul_f32_e32 v0, 0x43000000, v1
	v_mul_f32_e32 v1, 0x43000000, v5
	v_mul_f32_e32 v4, 0x43000000, v9
	ds_write_b128 v98, v[120:123]
	v_mov_b32_e32 v120, v153
	v_cvt_pk_fp8_f32 v120, v0, v1
	v_mul_f32_e32 v0, 0x43000000, v17
	v_mul_f32_e32 v1, 0x43000000, v21
	v_mov_b32_e32 v121, v153
	v_cvt_pk_fp8_f32 v121, v0, v1
	v_mul_f32_e32 v0, 0x43000000, v33
	v_mul_f32_e32 v1, 0x43000000, v37
	v_mov_b32_e32 v122, v153
	v_cvt_pk_fp8_f32 v122, v0, v1
	v_mul_f32_e32 v0, 0x43000000, v49
	v_mul_f32_e32 v1, 0x43000000, v53
	v_mov_b32_e32 v123, v153
	v_mul_f32_e32 v5, 0x43000000, v13
	v_cvt_pk_fp8_f32 v123, v0, v1
	v_cvt_pk_fp8_f32 v120, v4, v5 op_sel:[0,0,1]
	v_mul_f32_e32 v4, 0x43000000, v25
	v_mul_f32_e32 v5, 0x43000000, v29
	v_cvt_pk_fp8_f32 v121, v4, v5 op_sel:[0,0,1]
	v_mul_f32_e32 v4, 0x43000000, v41
	v_mul_f32_e32 v5, 0x43000000, v45
	v_cvt_pk_fp8_f32 v122, v4, v5 op_sel:[0,0,1]
	v_mul_f32_e32 v4, 0x43000000, v57
	v_mul_f32_e32 v5, 0x43000000, v117
	v_cvt_pk_fp8_f32 v123, v4, v5 op_sel:[0,0,1]
	v_mul_f32_e32 v0, 0x43000000, v2
	v_mul_f32_e32 v1, 0x43000000, v6
	v_mul_f32_e32 v2, 0x43000000, v10
	ds_write_b128 v98, v[120:123] offset:2560
	v_mov_b32_e32 v120, v153
	v_cvt_pk_fp8_f32 v120, v0, v1
	v_mul_f32_e32 v0, 0x43000000, v18
	v_mul_f32_e32 v1, 0x43000000, v22
	v_mov_b32_e32 v121, v153
	v_cvt_pk_fp8_f32 v121, v0, v1
	v_mul_f32_e32 v0, 0x43000000, v34
	v_mul_f32_e32 v1, 0x43000000, v38
	v_mov_b32_e32 v122, v153
	v_cvt_pk_fp8_f32 v122, v0, v1
	v_mul_f32_e32 v0, 0x43000000, v50
	v_mul_f32_e32 v1, 0x43000000, v54
	v_mov_b32_e32 v123, v153
	v_mul_f32_e32 v4, 0x43000000, v14
	v_cvt_pk_fp8_f32 v123, v0, v1
	v_cvt_pk_fp8_f32 v120, v2, v4 op_sel:[0,0,1]
	v_mul_f32_e32 v2, 0x43000000, v26
	v_mul_f32_e32 v4, 0x43000000, v30
	v_cvt_pk_fp8_f32 v121, v2, v4 op_sel:[0,0,1]
	v_mul_f32_e32 v2, 0x43000000, v42
	v_mul_f32_e32 v4, 0x43000000, v46
	v_cvt_pk_fp8_f32 v122, v2, v4 op_sel:[0,0,1]
	v_mul_f32_e32 v2, 0x43000000, v58
	v_mul_f32_e32 v4, 0x43000000, v118
	v_cvt_pk_fp8_f32 v123, v2, v4 op_sel:[0,0,1]
	v_mul_f32_e32 v1, 0x43000000, v3
	v_mul_f32_e32 v2, 0x43000000, v7
	v_mov_b32_e32 v0, v153
	v_cvt_pk_fp8_f32 v0, v1, v2
	v_mul_f32_e32 v3, 0x43000000, v11
	v_mul_f32_e32 v4, 0x43000000, v15
	v_mul_f32_e32 v2, 0x43000000, v19
	v_cvt_pk_fp8_f32 v0, v3, v4 op_sel:[0,0,1]
	v_mul_f32_e32 v3, 0x43000000, v23
	v_mov_b32_e32 v1, v153
	v_cvt_pk_fp8_f32 v1, v2, v3
	v_mul_f32_e32 v4, 0x43000000, v27
	v_mul_f32_e32 v5, 0x43000000, v31
	v_mul_f32_e32 v3, 0x43000000, v35
	v_cvt_pk_fp8_f32 v1, v4, v5 op_sel:[0,0,1]
	v_mul_f32_e32 v4, 0x43000000, v39
	v_mov_b32_e32 v2, v153
	v_cvt_pk_fp8_f32 v2, v3, v4
	v_mul_f32_e32 v5, 0x43000000, v43
	v_mul_f32_e32 v6, 0x43000000, v47
	v_mul_f32_e32 v4, 0x43000000, v51
	v_cvt_pk_fp8_f32 v2, v5, v6 op_sel:[0,0,1]
	v_mul_f32_e32 v5, 0x43000000, v55
	v_mov_b32_e32 v3, v153
	v_cvt_pk_fp8_f32 v3, v4, v5
	v_mul_f32_e32 v6, 0x43000000, v59
	v_mul_f32_e32 v7, 0x43000000, v119
	v_mov_b32_e32 v116, v153
	v_cvt_pk_fp8_f32 v3, v6, v7 op_sel:[0,0,1]
	v_mov_b32_e32 v117, v153
	v_mov_b32_e32 v118, v153
	v_mov_b32_e32 v119, v153
	ds_write_b128 v98, v[0:3] offset:7680
	v_add_co_u32_e32 v0, vcc, s2, v60
	s_mov_b32 s2, 0x42000
	s_nop 0
	v_addc_co_u32_e32 v1, vcc, 0, v61, vcc
	v_add_co_u32_e32 v4, vcc, s2, v60
	s_mov_b32 s2, 0x44000
	s_nop 0
	v_addc_co_u32_e32 v5, vcc, 0, v61, vcc
	v_add_co_u32_e32 v8, vcc, s2, v60
	s_mov_b32 s2, 0x46000
	s_nop 0
	v_addc_co_u32_e32 v9, vcc, 0, v61, vcc
	v_add_co_u32_e32 v12, vcc, s2, v60
	s_mov_b32 s2, 0x48000
	s_nop 0
	v_addc_co_u32_e32 v13, vcc, 0, v61, vcc
	global_load_dwordx4 v[8:11], v[8:9], off
	ds_write_b128 v98, v[120:123] offset:5120
	global_load_dwordx4 v[16:19], v[12:13], off
	v_add_co_u32_e32 v12, vcc, s2, v60
	s_mov_b32 s2, 0x4a000
	s_nop 0
	v_addc_co_u32_e32 v13, vcc, 0, v61, vcc
	v_add_co_u32_e32 v20, vcc, s2, v60
	s_mov_b32 s2, 0x4c000
	s_nop 0
	v_addc_co_u32_e32 v21, vcc, 0, v61, vcc
	global_load_dwordx4 v[12:15], v[12:13], off
	s_waitcnt vmcnt(0)
	v_mul_f32_e32 v8, 0x43000000, v8
	global_load_dwordx4 v[24:27], v[20:21], off
	v_add_co_u32_e32 v20, vcc, s2, v60
	s_mov_b32 s2, 0x4e000
	s_nop 0
	v_addc_co_u32_e32 v21, vcc, 0, v61, vcc
	global_load_dwordx4 v[28:31], v[20:21], off
	v_add_co_u32_e32 v20, vcc, s2, v60
	s_mov_b32 s2, 0x50000
	s_nop 0
	v_addc_co_u32_e32 v21, vcc, 0, v61, vcc
	global_load_dwordx4 v[40:43], v[20:21], off
	v_add_co_u32_e32 v20, vcc, s2, v60
	s_mov_b32 s2, 0x52000
	s_nop 0
	v_addc_co_u32_e32 v21, vcc, 0, v61, vcc
	v_add_co_u32_e32 v32, vcc, s2, v60
	s_mov_b32 s2, 0x54000
	s_nop 0
	v_addc_co_u32_e32 v33, vcc, 0, v61, vcc
	v_add_co_u32_e32 v36, vcc, s2, v60
	s_mov_b32 s2, 0x56000
	s_nop 0
	v_addc_co_u32_e32 v37, vcc, 0, v61, vcc
	v_add_co_u32_e32 v44, vcc, s2, v60
	s_mov_b32 s2, 0x58000
	s_nop 0
	v_addc_co_u32_e32 v45, vcc, 0, v61, vcc
	global_load_dwordx4 v[36:39], v[36:37], off
	s_waitcnt vmcnt(5)
	v_mul_f32_e32 v16, 0x43000000, v16
	global_load_dwordx4 v[48:51], v[44:45], off
	v_add_co_u32_e32 v44, vcc, s2, v60
	global_load_dwordx4 v[0:3], v[0:1], off
	s_nop 0
	v_addc_co_u32_e32 v45, vcc, 0, v61, vcc
	global_load_dwordx4 v[4:7], v[4:5], off
	s_mov_b32 s2, 0x5a000
	v_add_co_u32_e32 v52, vcc, s2, v60
	global_load_dwordx4 v[20:23], v[20:21], off
	s_nop 0
	v_addc_co_u32_e32 v53, vcc, 0, v61, vcc
	global_load_dwordx4 v[32:35], v[32:33], off
	s_mov_b32 s2, 0x5c000
	global_load_dwordx4 v[44:47], v[44:45], off
	v_add_co_u32_e32 v56, vcc, s2, v60
	global_load_dwordx4 v[52:55], v[52:53], off
	s_nop 0
	v_addc_co_u32_e32 v57, vcc, 0, v61, vcc
	s_mov_b32 s2, 0x5e000
	v_add_co_u32_e32 v60, vcc, s2, v60
	global_load_dwordx4 v[56:59], v[56:57], off
	s_nop 0
	v_addc_co_u32_e32 v61, vcc, 0, v61, vcc
	global_load_dwordx4 v[60:63], v[60:61], off
	s_waitcnt vmcnt(0)
; #define LAS __attribute__((address_space(3)))
; __device__ __forceinline__ unsigned pk4_fp8(float x0, float x1, float x2, float x3) { int w = 0; w = __builtin_amdgcn_cvt_pk_fp8_f32(x0, x1, w, false); w = __builtin_amdgcn_cvt_pk_fp8_f32(x2, x3, w, true); return (unsigned)w; }
; __device__ __forceinline__ void transpose_item_fp8w(const float* W, int K, int N, unsigned char* WT, float q, LAS unsigned char* scr, int item, int lane) {
;     ...
; #pragma unroll
;         for (int i = 0; i < 4; ++i) {
;             u32x4 o;
;             o.x = pk4_fp8(x[0][i] * q, x[1][i] * q, x[2][i] * q, x[3][i] * q); o.y = pk4_fp8(x[4][i] * q, x[5][i] * q, x[6][i] * q, x[7][i] * q);
;             o.z = pk4_fp8(x[8][i] * q, x[9][i] * q, x[10][i] * q, x[11][i] * q); o.w = pk4_fp8(x[12][i] * q, x[13][i] * q, x[14][i] * q, x[15][i] * q);
;             *(LAS u32x4*)(scr + (l5 + 32 * i) * 80 + (2 * b + h) * 16) = o; }
;     }
;     asm volatile("s_waitcnt lgkmcnt(0)" ::: "memory");
; #pragma unroll
;     for (int qd = 0; qd < 8; ++qd) {
;         const int rho = 16 * qd + (lane >> 2), piece = lane & 3;
;         const u32x4 o = *(const LAS u32x4*)(scr + rho * 80 + piece * 16);
;         const int nl = 4 * (rho & 31) + (rho >> 5);
;         *(u32x4*)(WT + (size_t)(n0 + nl) * K + k0 + piece * 16) = o; }
;     asm volatile("s_waitcnt lgkmcnt(0)" ::: "memory");
	v_mul_f32_e32 v0, 0x43000000, v0
	s_waitcnt vmcnt(6)
	v_mul_f32_e32 v4, 0x43000000, v4
	v_cvt_pk_fp8_f32 v116, v0, v4
	v_mul_f32_e32 v0, 0x43000000, v12
	v_mul_f32_e32 v4, 0x43000000, v24
	v_cvt_pk_fp8_f32 v117, v0, v4
	s_waitcnt vmcnt(5)
	v_mul_f32_e32 v0, 0x43000000, v20
	v_cvt_pk_fp8_f32 v116, v8, v16 op_sel:[0,0,1]
	s_waitcnt vmcnt(4)
	v_mul_f32_e32 v4, 0x43000000, v32
	v_cvt_pk_fp8_f32 v118, v0, v4
	s_waitcnt vmcnt(3)
	v_mul_f32_e32 v0, 0x43000000, v44
	v_mul_f32_e32 v8, 0x43000000, v28
	v_mul_f32_e32 v12, 0x43000000, v40
	s_waitcnt vmcnt(2)
	v_mul_f32_e32 v4, 0x43000000, v52
	v_cvt_pk_fp8_f32 v119, v0, v4
	v_cvt_pk_fp8_f32 v117, v8, v12 op_sel:[0,0,1]
	v_mul_f32_e32 v8, 0x43000000, v36
	v_mul_f32_e32 v12, 0x43000000, v48
	v_cvt_pk_fp8_f32 v118, v8, v12 op_sel:[0,0,1]
	s_waitcnt vmcnt(1)
	v_mul_f32_e32 v8, 0x43000000, v56
	v_mul_f32_e32 v0, 0x43000000, v1
	v_mul_f32_e32 v1, 0x43000000, v5
	s_waitcnt vmcnt(0)
	v_mul_f32_e32 v12, 0x43000000, v60
	v_cvt_pk_fp8_f32 v119, v8, v12 op_sel:[0,0,1]
	v_mul_f32_e32 v4, 0x43000000, v9
	v_mul_f32_e32 v5, 0x43000000, v17
	ds_write_b128 v98, v[116:119] offset:32
	v_mov_b32_e32 v116, v153
	v_cvt_pk_fp8_f32 v116, v0, v1
	v_mul_f32_e32 v0, 0x43000000, v13
	v_mul_f32_e32 v1, 0x43000000, v25
	v_mov_b32_e32 v117, v153
	v_cvt_pk_fp8_f32 v117, v0, v1
	v_mul_f32_e32 v0, 0x43000000, v21
	v_mul_f32_e32 v1, 0x43000000, v33
	v_mov_b32_e32 v118, v153
	v_cvt_pk_fp8_f32 v118, v0, v1
	v_mul_f32_e32 v0, 0x43000000, v45
	v_mul_f32_e32 v1, 0x43000000, v53
	v_mov_b32_e32 v119, v153
	v_cvt_pk_fp8_f32 v119, v0, v1
	v_cvt_pk_fp8_f32 v116, v4, v5 op_sel:[0,0,1]
	v_mul_f32_e32 v4, 0x43000000, v29
	v_mul_f32_e32 v5, 0x43000000, v41
	v_cvt_pk_fp8_f32 v117, v4, v5 op_sel:[0,0,1]
	v_mul_f32_e32 v4, 0x43000000, v37
	v_mul_f32_e32 v5, 0x43000000, v49
	v_cvt_pk_fp8_f32 v118, v4, v5 op_sel:[0,0,1]
	v_mul_f32_e32 v4, 0x43000000, v57
	v_mul_f32_e32 v5, 0x43000000, v61
	v_cvt_pk_fp8_f32 v119, v4, v5 op_sel:[0,0,1]
	v_mul_f32_e32 v0, 0x43000000, v2
	v_mul_f32_e32 v1, 0x43000000, v6
	v_mul_f32_e32 v2, 0x43000000, v10
	ds_write_b128 v98, v[116:119] offset:2592
	v_mov_b32_e32 v116, v153
	v_cvt_pk_fp8_f32 v116, v0, v1
	v_mul_f32_e32 v0, 0x43000000, v14
	v_mul_f32_e32 v1, 0x43000000, v26
	v_mov_b32_e32 v117, v153
	v_cvt_pk_fp8_f32 v117, v0, v1
	v_mul_f32_e32 v0, 0x43000000, v22
	v_mul_f32_e32 v1, 0x43000000, v34
	v_mov_b32_e32 v118, v153
	v_cvt_pk_fp8_f32 v118, v0, v1
	v_mul_f32_e32 v0, 0x43000000, v46
	v_mul_f32_e32 v1, 0x43000000, v54
	v_mov_b32_e32 v119, v153
	v_mul_f32_e32 v4, 0x43000000, v18
	v_cvt_pk_fp8_f32 v119, v0, v1
	v_cvt_pk_fp8_f32 v116, v2, v4 op_sel:[0,0,1]
	v_mul_f32_e32 v2, 0x43000000, v30
	v_mul_f32_e32 v4, 0x43000000, v42
	v_cvt_pk_fp8_f32 v117, v2, v4 op_sel:[0,0,1]
	v_mul_f32_e32 v2, 0x43000000, v38
	v_mul_f32_e32 v4, 0x43000000, v50
	v_cvt_pk_fp8_f32 v118, v2, v4 op_sel:[0,0,1]
	v_mul_f32_e32 v2, 0x43000000, v58
	v_mul_f32_e32 v4, 0x43000000, v62
	v_cvt_pk_fp8_f32 v119, v2, v4 op_sel:[0,0,1]
	v_mul_f32_e32 v1, 0x43000000, v3
	v_mul_f32_e32 v2, 0x43000000, v7
	v_mov_b32_e32 v0, v153
	v_cvt_pk_fp8_f32 v0, v1, v2
	v_mul_f32_e32 v3, 0x43000000, v11
	v_mul_f32_e32 v4, 0x43000000, v19
	v_mul_f32_e32 v2, 0x43000000, v15
	v_cvt_pk_fp8_f32 v0, v3, v4 op_sel:[0,0,1]
	v_mul_f32_e32 v3, 0x43000000, v27
	v_mov_b32_e32 v1, v153
	v_cvt_pk_fp8_f32 v1, v2, v3
	v_mul_f32_e32 v4, 0x43000000, v31
	v_mul_f32_e32 v5, 0x43000000, v43
	v_mul_f32_e32 v3, 0x43000000, v23
	v_cvt_pk_fp8_f32 v1, v4, v5 op_sel:[0,0,1]
	v_mul_f32_e32 v4, 0x43000000, v35
	v_mov_b32_e32 v2, v153
	v_cvt_pk_fp8_f32 v2, v3, v4
	v_mul_f32_e32 v5, 0x43000000, v39
	v_mul_f32_e32 v6, 0x43000000, v51
	v_mul_f32_e32 v4, 0x43000000, v47
	v_cvt_pk_fp8_f32 v2, v5, v6 op_sel:[0,0,1]
	v_mul_f32_e32 v5, 0x43000000, v55
	v_mov_b32_e32 v3, v153
	v_cvt_pk_fp8_f32 v3, v4, v5
	v_mul_f32_e32 v6, 0x43000000, v59
	v_mul_f32_e32 v7, 0x43000000, v63
	ds_write_b128 v98, v[116:119] offset:5152
	v_cvt_pk_fp8_f32 v3, v6, v7 op_sel:[0,0,1]
	v_add_u32_e32 v6, s0, v102
	v_ashrrev_i32_e32 v7, 31, v6
	v_lshl_add_u64 v[4:5], s[10:11], 0, v[64:65]
	ds_write_b128 v98, v[0:3] offset:7712
	s_waitcnt lgkmcnt(0)
	ds_read_b128 v[0:3], v99
	v_lshlrev_b64 v[6:7], 10, v[6:7]
	v_lshl_add_u64 v[6:7], v[4:5], 0, v[6:7]
	s_waitcnt lgkmcnt(0)
	global_store_dwordx4 v[6:7], v[0:3], off
	ds_read_b128 v[0:3], v99 offset:1280
	v_add_u32_e32 v6, s0, v103
	v_ashrrev_i32_e32 v7, 31, v6
	v_lshlrev_b64 v[6:7], 10, v[6:7]
	v_lshl_add_u64 v[6:7], v[4:5], 0, v[6:7]
	s_waitcnt lgkmcnt(0)
	global_store_dwordx4 v[6:7], v[0:3], off
	ds_read_b128 v[0:3], v99 offset:2560
	v_add_u32_e32 v6, s0, v104
	v_ashrrev_i32_e32 v7, 31, v6
	v_lshlrev_b64 v[6:7], 10, v[6:7]
	v_lshl_add_u64 v[6:7], v[4:5], 0, v[6:7]
	s_waitcnt lgkmcnt(0)
	global_store_dwordx4 v[6:7], v[0:3], off
	ds_read_b128 v[0:3], v99 offset:3840
	v_add_u32_e32 v6, s0, v105
	v_ashrrev_i32_e32 v7, 31, v6
	v_lshlrev_b64 v[6:7], 10, v[6:7]
	v_lshl_add_u64 v[6:7], v[4:5], 0, v[6:7]
	s_waitcnt lgkmcnt(0)
	global_store_dwordx4 v[6:7], v[0:3], off
	ds_read_b128 v[0:3], v99 offset:5120
	v_add_u32_e32 v6, s0, v106
	v_ashrrev_i32_e32 v7, 31, v6
	v_lshlrev_b64 v[6:7], 10, v[6:7]
	v_lshl_add_u64 v[6:7], v[4:5], 0, v[6:7]
	s_waitcnt lgkmcnt(0)
	global_store_dwordx4 v[6:7], v[0:3], off
	ds_read_b128 v[0:3], v99 offset:6400
	v_add_u32_e32 v6, s0, v107
	v_ashrrev_i32_e32 v7, 31, v6
	v_lshlrev_b64 v[6:7], 10, v[6:7]
	v_lshl_add_u64 v[6:7], v[4:5], 0, v[6:7]
	s_waitcnt lgkmcnt(0)
	global_store_dwordx4 v[6:7], v[0:3], off
	ds_read_b128 v[0:3], v99 offset:7680
	v_add_u32_e32 v6, s0, v108
	v_ashrrev_i32_e32 v7, 31, v6
	v_lshlrev_b64 v[6:7], 10, v[6:7]
	v_lshl_add_u64 v[6:7], v[4:5], 0, v[6:7]
	s_waitcnt lgkmcnt(0)
	global_store_dwordx4 v[6:7], v[0:3], off
	ds_read_b128 v[0:3], v99 offset:8960
	v_add_u32_e32 v6, s0, v109
	v_ashrrev_i32_e32 v7, 31, v6
	v_lshlrev_b64 v[6:7], 10, v[6:7]
	v_lshl_add_u64 v[4:5], v[4:5], 0, v[6:7]
	s_waitcnt lgkmcnt(0)
	global_store_dwordx4 v[4:5], v[0:3], off
	s_waitcnt lgkmcnt(0)
	s_mov_b64 s[0:1], 0

; #define LAS __attribute__((address_space(3)))
; __device__ __forceinline__ unsigned pk4_fp8(float x0, float x1, float x2, float x3) { int w = 0; w = __builtin_amdgcn_cvt_pk_fp8_f32(x0, x1, w, false); w = __builtin_amdgcn_cvt_pk_fp8_f32(x2, x3, w, true); return (unsigned)w; }
; __device__ __forceinline__ void transpose_item_fp8w(const float* W, int K, int N, unsigned char* WT, float q, LAS unsigned char* scr, int item, int lane) {
;     const int nblk = N / 128, kb = item / nblk, nb = item % nblk, k0 = 64 * kb, n0 = 128 * nb;
;     const int l5 = lane & 31, h = lane >> 5;
;     const float* src = W + (size_t)(k0 + 16 * h) * N + n0 + 4 * l5;
; #pragma unroll
;     for (int b = 0; b < 2; ++b) {
;         f32x4 x[16];
; #pragma unroll
;         for (int s_ = 0; s_ < 16; ++s_) x[s_] = *(const f32x4*)(src + (size_t)(32 * b + s_) * N);
; #pragma unroll
;         for (int i = 0; i < 4; ++i) {
;             u32x4 o;
;             o.x = pk4_fp8(x[0][i] * q, x[1][i] * q, x[2][i] * q, x[3][i] * q); o.y = pk4_fp8(x[4][i] * q, x[5][i] * q, x[6][i] * q, x[7][i] * q);
;             o.z = pk4_fp8(x[8][i] * q, x[9][i] * q, x[10][i] * q, x[11][i] * q); o.w = pk4_fp8(x[12][i] * q, x[13][i] * q, x[14][i] * q, x[15][i] * q);
;             *(LAS u32x4*)(scr + (l5 + 32 * i) * 80 + (2 * b + h) * 16) = o; }
.LBB0_662:
	s_cmpk_gt_i32 s5, 0x3df
	s_mov_b64 s[0:1], -1
	s_cbranch_scc0 .LBB0_694
	s_cmpk_gt_u32 s5, 0x46f
	s_cbranch_scc0 .LBB0_681
	s_cmpk_gt_u32 s5, 0x4ef
	s_cbranch_scc0 .LBB0_676
	s_cmpk_gt_u32 s5, 0x6ef
	s_cbranch_scc0 .LBB0_671
	s_cmpk_gt_u32 s5, 0x26ef
	v_lshlrev_b32_e32 v152, 2, v64
	v_add_u32_e32 v118, v102, v103
	s_cbranch_scc0 .LBB0_668
	s_add_i32 s4, s5, 0xffffd910
	v_readlane_b32 s2, v253, 32
	s_lshr_b32 s0, s4, 7
	v_readlane_b32 s3, v253, 33
	s_mov_b32 s11, s3
	s_add_i32 s10, s0, s56
	v_readlane_b32 s40, v253, 58
	s_lshl_b64 s[2:3], s[10:11], 20
	s_lshl_b64 s[0:1], s[10:11], 22
	v_readlane_b32 s54, v254, 8
	v_readlane_b32 s55, v254, 9
	s_add_u32 s8, s54, s0
	s_addc_u32 s9, s55, s1
	v_readlane_b32 s0, v246, 17
	s_add_u32 s1, s0, s2
	v_readlane_b32 s0, v246, 18
	s_addc_u32 s6, s0, s3
	s_lshl_b32 s0, s4, 6
	s_and_b32 s7, s0, 0x3c0
	v_add_u32_e32 v0, s7, v99
	s_lshl_b32 s0, s4, 3
	v_ashrrev_i32_e32 v1, 31, v0
	s_and_b32 s0, s0, 0x380
	v_lshlrev_b64 v[0:1], 12, v[0:1]
	v_lshl_add_u64 v[0:1], s[8:9], 0, v[0:1]
	s_lshl_b32 s10, s0, 2
	s_mov_b32 s3, s11
	v_readlane_b32 s41, v253, 59
	v_readlane_b32 s42, v253, 60
	v_readlane_b32 s43, v253, 61
	v_readlane_b32 s44, v253, 62
	v_readlane_b32 s45, v253, 63
	v_writelane_b32 v253, s2, 32
	v_lshl_add_u64 v[0:1], v[0:1], 0, s[10:11]
	v_lshl_add_u64 v[100:101], v[0:1], 0, v[152:153]
	v_writelane_b32 v253, s3, 33
	s_movk_i32 s2, 0x2000
	v_add_co_u32_e32 v8, vcc, s2, v100
	s_movk_i32 s2, 0x4000
	s_nop 0
	v_addc_co_u32_e32 v9, vcc, 0, v101, vcc
	v_add_co_u32_e32 v12, vcc, s2, v100
	s_movk_i32 s2, 0x6000
	s_nop 0
	v_addc_co_u32_e32 v13, vcc, 0, v101, vcc
	v_add_co_u32_e32 v24, vcc, s2, v100
	s_mov_b32 s2, 0x8000
	s_nop 0
	v_addc_co_u32_e32 v25, vcc, 0, v101, vcc
	v_add_co_u32_e32 v28, vcc, s2, v100
	s_mov_b32 s2, 0xa000
	s_nop 0
	v_addc_co_u32_e32 v29, vcc, 0, v101, vcc
	v_add_co_u32_e32 v40, vcc, s2, v100
	s_mov_b32 s2, 0xc000
	s_nop 0
	v_addc_co_u32_e32 v41, vcc, 0, v101, vcc
	global_load_dwordx4 v[0:3], v[100:101], off
	v_add_co_u32_e32 v44, vcc, s2, v100
	global_load_dwordx4 v[4:7], v[8:9], off offset:-4096
	s_nop 0
	global_load_dwordx4 v[8:11], v[8:9], off
	s_nop 0
	global_load_dwordx4 v[16:19], v[12:13], off offset:-4096
	s_nop 0
	global_load_dwordx4 v[12:15], v[12:13], off
	v_addc_co_u32_e32 v45, vcc, 0, v101, vcc
	s_mov_b32 s2, 0xe000
	global_load_dwordx4 v[20:23], v[24:25], off offset:-4096
	s_nop 0
	global_load_dwordx4 v[24:27], v[24:25], off
	s_nop 0
	global_load_dwordx4 v[32:35], v[28:29], off offset:-4096
	s_nop 0
	global_load_dwordx4 v[28:31], v[28:29], off
	v_add_co_u32_e32 v56, vcc, s2, v100
	global_load_dwordx4 v[36:39], v[40:41], off offset:-4096
	s_nop 0
	global_load_dwordx4 v[40:43], v[40:41], off
	s_nop 0
	global_load_dwordx4 v[48:51], v[44:45], off offset:-4096
	s_nop 0
	global_load_dwordx4 v[44:47], v[44:45], off
	v_addc_co_u32_e32 v57, vcc, 0, v101, vcc
	global_load_dwordx4 v[52:55], v[56:57], off offset:-4096
	s_nop 0
	global_load_dwordx4 v[56:59], v[56:57], off
	s_mov_b32 s2, 0xf000
	v_add_co_u32_e32 v60, vcc, s2, v100
	v_mov_b32_e32 v120, v153
	s_nop 0
	v_addc_co_u32_e32 v61, vcc, 0, v101, vcc
	global_load_dwordx4 v[60:63], v[60:61], off
	v_mov_b32_e32 v121, v153
	v_mov_b32_e32 v122, v153
	v_mov_b32_e32 v123, v153
	s_mov_b32 s2, 0x21000
	v_readlane_b32 s46, v254, 0
	v_readlane_b32 s47, v254, 1
	v_readlane_b32 s48, v254, 2
	v_readlane_b32 s49, v254, 3
	v_readlane_b32 s50, v254, 4
	v_readlane_b32 s51, v254, 5
	v_readlane_b32 s52, v254, 6
	v_readlane_b32 s53, v254, 7
	s_waitcnt vmcnt(0)
	v_mul_f32_e32 v0, 0x43800000, v0
	v_mul_f32_e32 v4, 0x43800000, v4
	v_cvt_pk_fp8_f32 v120, v0, v4
	v_mul_f32_e32 v0, 0x43800000, v12
	v_mul_f32_e32 v8, 0x43800000, v8
	v_mul_f32_e32 v16, 0x43800000, v16
	v_mul_f32_e32 v4, 0x43800000, v20
	v_cvt_pk_fp8_f32 v121, v0, v4
	v_mul_f32_e32 v0, 0x43800000, v28
	v_cvt_pk_fp8_f32 v120, v8, v16 op_sel:[0,0,1]
	v_mul_f32_e32 v4, 0x43800000, v36
	v_cvt_pk_fp8_f32 v122, v0, v4
	v_mul_f32_e32 v0, 0x43800000, v44
	v_mul_f32_e32 v8, 0x43800000, v24
	v_mul_f32_e32 v4, 0x43800000, v52
	v_cvt_pk_fp8_f32 v123, v0, v4
	v_mul_f32_e32 v12, 0x43800000, v32
	v_cvt_pk_fp8_f32 v121, v8, v12 op_sel:[0,0,1]
	v_mul_f32_e32 v8, 0x43800000, v40
	v_mul_f32_e32 v12, 0x43800000, v48
	v_cvt_pk_fp8_f32 v122, v8, v12 op_sel:[0,0,1]
	v_mul_f32_e32 v8, 0x43800000, v56
	v_mul_f32_e32 v12, 0x43800000, v60
	v_cvt_pk_fp8_f32 v123, v8, v12 op_sel:[0,0,1]
	v_mul_f32_e32 v0, 0x43800000, v1
	v_mul_f32_e32 v1, 0x43800000, v5
	v_mul_f32_e32 v4, 0x43800000, v9
	ds_write_b128 v117, v[120:123]
	v_mov_b32_e32 v120, v153
	v_cvt_pk_fp8_f32 v120, v0, v1
	v_mul_f32_e32 v0, 0x43800000, v13
	v_mul_f32_e32 v1, 0x43800000, v21
	v_mov_b32_e32 v121, v153
	v_cvt_pk_fp8_f32 v121, v0, v1
	v_mul_f32_e32 v0, 0x43800000, v29
	v_mul_f32_e32 v1, 0x43800000, v37
	v_mov_b32_e32 v122, v153
	v_cvt_pk_fp8_f32 v122, v0, v1
	v_mul_f32_e32 v0, 0x43800000, v45
	v_mul_f32_e32 v1, 0x43800000, v53
	v_mov_b32_e32 v123, v153
	v_mul_f32_e32 v5, 0x43800000, v17
	v_cvt_pk_fp8_f32 v123, v0, v1
	v_cvt_pk_fp8_f32 v120, v4, v5 op_sel:[0,0,1]
	v_mul_f32_e32 v4, 0x43800000, v25
	v_mul_f32_e32 v5, 0x43800000, v33
	v_cvt_pk_fp8_f32 v121, v4, v5 op_sel:[0,0,1]
	v_mul_f32_e32 v4, 0x43800000, v41
	v_mul_f32_e32 v5, 0x43800000, v49
	v_cvt_pk_fp8_f32 v122, v4, v5 op_sel:[0,0,1]
	v_mul_f32_e32 v4, 0x43800000, v57
	v_mul_f32_e32 v5, 0x43800000, v61
	v_cvt_pk_fp8_f32 v123, v4, v5 op_sel:[0,0,1]
	v_mul_f32_e32 v0, 0x43800000, v2
	v_mul_f32_e32 v1, 0x43800000, v6
	v_mul_f32_e32 v2, 0x43800000, v10
	ds_write_b128 v117, v[120:123] offset:2560
	v_mov_b32_e32 v120, v153
	v_cvt_pk_fp8_f32 v120, v0, v1
	v_mul_f32_e32 v0, 0x43800000, v14
; #define LAS __attribute__((address_space(3)))
; __device__ __forceinline__ unsigned pk4_fp8(float x0, float x1, float x2, float x3) { int w = 0; w = __builtin_amdgcn_cvt_pk_fp8_f32(x0, x1, w, false); w = __builtin_amdgcn_cvt_pk_fp8_f32(x2, x3, w, true); return (unsigned)w; }
; __device__ __forceinline__ void transpose_item_fp8w(const float* W, int K, int N, unsigned char* WT, float q, LAS unsigned char* scr, int item, int lane) {
;     ...
;     for (int b = 0; b < 2; ++b) {
;         f32x4 x[16];
; #pragma unroll
;         for (int s_ = 0; s_ < 16; ++s_) x[s_] = *(const f32x4*)(src + (size_t)(32 * b + s_) * N);
; #pragma unroll
;         for (int i = 0; i < 4; ++i) {
;             u32x4 o;
;             o.x = pk4_fp8(x[0][i] * q, x[1][i] * q, x[2][i] * q, x[3][i] * q); o.y = pk4_fp8(x[4][i] * q, x[5][i] * q, x[6][i] * q, x[7][i] * q);
;             o.z = pk4_fp8(x[8][i] * q, x[9][i] * q, x[10][i] * q, x[11][i] * q); o.w = pk4_fp8(x[12][i] * q, x[13][i] * q, x[14][i] * q, x[15][i] * q);
;             *(LAS u32x4*)(scr + (l5 + 32 * i) * 80 + (2 * b + h) * 16) = o; }
	v_mul_f32_e32 v1, 0x43800000, v22
	v_mov_b32_e32 v121, v153
	v_cvt_pk_fp8_f32 v121, v0, v1
	v_mul_f32_e32 v0, 0x43800000, v30
	v_mul_f32_e32 v1, 0x43800000, v38
	v_mov_b32_e32 v122, v153
	v_cvt_pk_fp8_f32 v122, v0, v1
	v_mul_f32_e32 v0, 0x43800000, v46
	v_mul_f32_e32 v1, 0x43800000, v54
	v_mov_b32_e32 v123, v153
	v_mul_f32_e32 v4, 0x43800000, v18
	v_cvt_pk_fp8_f32 v123, v0, v1
	v_cvt_pk_fp8_f32 v120, v2, v4 op_sel:[0,0,1]
	v_mul_f32_e32 v2, 0x43800000, v26
	v_mul_f32_e32 v4, 0x43800000, v34
	v_cvt_pk_fp8_f32 v121, v2, v4 op_sel:[0,0,1]
	v_mul_f32_e32 v2, 0x43800000, v42
	v_mul_f32_e32 v4, 0x43800000, v50
	v_cvt_pk_fp8_f32 v122, v2, v4 op_sel:[0,0,1]
	v_mul_f32_e32 v2, 0x43800000, v58
	v_mul_f32_e32 v4, 0x43800000, v62
	v_cvt_pk_fp8_f32 v123, v2, v4 op_sel:[0,0,1]
	v_mul_f32_e32 v1, 0x43800000, v3
	v_mul_f32_e32 v2, 0x43800000, v7
	v_mov_b32_e32 v0, v153
	v_cvt_pk_fp8_f32 v0, v1, v2
	v_mul_f32_e32 v3, 0x43800000, v11
	v_mul_f32_e32 v4, 0x43800000, v19
	v_mul_f32_e32 v2, 0x43800000, v15
	v_cvt_pk_fp8_f32 v0, v3, v4 op_sel:[0,0,1]
	v_mul_f32_e32 v3, 0x43800000, v23
	v_mov_b32_e32 v1, v153
	v_cvt_pk_fp8_f32 v1, v2, v3
	v_mul_f32_e32 v4, 0x43800000, v27
	v_mul_f32_e32 v5, 0x43800000, v35
	v_mul_f32_e32 v3, 0x43800000, v31
	v_cvt_pk_fp8_f32 v1, v4, v5 op_sel:[0,0,1]
	v_mul_f32_e32 v4, 0x43800000, v39
	v_mov_b32_e32 v2, v153
	v_cvt_pk_fp8_f32 v2, v3, v4
	v_mul_f32_e32 v5, 0x43800000, v43
	v_mul_f32_e32 v6, 0x43800000, v51
	v_mul_f32_e32 v4, 0x43800000, v47
	v_cvt_pk_fp8_f32 v2, v5, v6 op_sel:[0,0,1]
	v_mul_f32_e32 v5, 0x43800000, v55
	v_mov_b32_e32 v3, v153
	v_cvt_pk_fp8_f32 v3, v4, v5
	v_mul_f32_e32 v6, 0x43800000, v59
	v_mul_f32_e32 v7, 0x43800000, v63
	ds_write_b128 v117, v[120:123] offset:5120
	v_cvt_pk_fp8_f32 v3, v6, v7 op_sel:[0,0,1]
	v_mov_b32_e32 v120, v153
	v_mov_b32_e32 v122, v153
	v_mov_b32_e32 v121, v153
	ds_write_b128 v117, v[0:3] offset:7680
	v_add_co_u32_e32 v0, vcc, s2, v100
	s_mov_b32 s2, 0x23000
	s_nop 0
	v_addc_co_u32_e32 v1, vcc, 0, v101, vcc
	global_load_dwordx4 v[32:35], v[0:1], off offset:-4096
	global_load_dwordx4 v[36:39], v[0:1], off
	v_add_co_u32_e32 v0, vcc, s2, v100
	s_mov_b32 s2, 0x25000
	s_nop 0
	v_addc_co_u32_e32 v1, vcc, 0, v101, vcc
	global_load_dwordx4 v[48:51], v[0:1], off offset:-4096
	global_load_dwordx4 v[52:55], v[0:1], off
	v_add_co_u32_e32 v0, vcc, s2, v100
	s_mov_b32 s2, 0x27000
	s_nop 0
	v_addc_co_u32_e32 v1, vcc, 0, v101, vcc
	global_load_dwordx4 v[40:43], v[0:1], off offset:-4096
	global_load_dwordx4 v[44:47], v[0:1], off
	v_add_co_u32_e32 v0, vcc, s2, v100
	s_mov_b32 s2, 0x29000
	s_nop 0
	v_addc_co_u32_e32 v1, vcc, 0, v101, vcc
	v_add_co_u32_e32 v4, vcc, s2, v100
	s_mov_b32 s2, 0x2b000
	s_nop 0
	v_addc_co_u32_e32 v5, vcc, 0, v101, vcc
	v_add_co_u32_e32 v8, vcc, s2, v100
	s_mov_b32 s2, 0x2d000
	s_nop 0
	v_addc_co_u32_e32 v9, vcc, 0, v101, vcc
	v_add_co_u32_e32 v12, vcc, s2, v100
	global_load_dwordx4 v[56:59], v[0:1], off offset:-4096
	global_load_dwordx4 v[60:63], v[0:1], off
	s_nop 0
	global_load_dwordx4 v[0:3], v[4:5], off offset:-4096
	s_nop 0
	global_load_dwordx4 v[4:7], v[4:5], off
	v_addc_co_u32_e32 v13, vcc, 0, v101, vcc
	global_load_dwordx4 v[16:19], v[8:9], off offset:-4096
	global_load_dwordx4 v[20:23], v[8:9], off
	s_nop 0
	global_load_dwordx4 v[8:11], v[12:13], off offset:-4096
	s_nop 0
	global_load_dwordx4 v[12:15], v[12:13], off
	s_mov_b32 s2, 0x2f000
	v_add_co_u32_e32 v28, vcc, s2, v100
	v_mov_b32_e32 v123, v153
	s_nop 0
	v_addc_co_u32_e32 v29, vcc, 0, v101, vcc
	global_load_dwordx4 v[24:27], v[28:29], off offset:-4096
	s_nop 0
	global_load_dwordx4 v[28:31], v[28:29], off
	s_add_u32 s2, s1, s7
	s_addc_u32 s3, s6, 0
	s_waitcnt vmcnt(0)
	v_mul_f32_e32 v32, 0x43800000, v32
	s_waitcnt vmcnt(14)
	v_mul_f32_e32 v36, 0x43800000, v36
	v_cvt_pk_fp8_f32 v120, v32, v36
	s_waitcnt vmcnt(13)
	v_mul_f32_e32 v48, 0x43800000, v48
	s_waitcnt vmcnt(12)
	v_mul_f32_e32 v52, 0x43800000, v52
	v_cvt_pk_fp8_f32 v120, v48, v52 op_sel:[0,0,1]
	s_waitcnt vmcnt(11)
	v_mul_f32_e32 v32, 0x43800000, v40
	s_waitcnt vmcnt(10)
	v_mul_f32_e32 v36, 0x43800000, v44
	v_cvt_pk_fp8_f32 v121, v32, v36
	s_waitcnt vmcnt(9)
	v_mul_f32_e32 v40, 0x43800000, v56
	s_waitcnt vmcnt(7)
	v_mul_f32_e32 v0, 0x43800000, v0
	s_waitcnt vmcnt(6)
	v_mul_f32_e32 v4, 0x43800000, v4
	v_cvt_pk_fp8_f32 v122, v0, v4
	v_mul_f32_e32 v44, 0x43800000, v60
	s_waitcnt vmcnt(3)
	v_mul_f32_e32 v0, 0x43800000, v8
	s_waitcnt vmcnt(2)
	v_mul_f32_e32 v4, 0x43800000, v12
	v_cvt_pk_fp8_f32 v123, v0, v4
	v_mul_f32_e32 v16, 0x43800000, v16
	v_mul_f32_e32 v20, 0x43800000, v20
	v_cvt_pk_fp8_f32 v121, v40, v44 op_sel:[0,0,1]
	v_cvt_pk_fp8_f32 v122, v16, v20 op_sel:[0,0,1]
	s_waitcnt vmcnt(1)
	v_mul_f32_e32 v8, 0x43800000, v24
	s_waitcnt vmcnt(0)
; #define LAS __attribute__((address_space(3)))
; __device__ __forceinline__ unsigned pk4_fp8(float x0, float x1, float x2, float x3) { int w = 0; w = __builtin_amdgcn_cvt_pk_fp8_f32(x0, x1, w, false); w = __builtin_amdgcn_cvt_pk_fp8_f32(x2, x3, w, true); return (unsigned)w; }
; __device__ __forceinline__ void transpose_item_fp8w(const float* W, int K, int N, unsigned char* WT, float q, LAS unsigned char* scr, int item, int lane) {
;     ...
; #pragma unroll
;         for (int i = 0; i < 4; ++i) {
;             u32x4 o;
;             o.x = pk4_fp8(x[0][i] * q, x[1][i] * q, x[2][i] * q, x[3][i] * q); o.y = pk4_fp8(x[4][i] * q, x[5][i] * q, x[6][i] * q, x[7][i] * q);
;             o.z = pk4_fp8(x[8][i] * q, x[9][i] * q, x[10][i] * q, x[11][i] * q); o.w = pk4_fp8(x[12][i] * q, x[13][i] * q, x[14][i] * q, x[15][i] * q);
;             *(LAS u32x4*)(scr + (l5 + 32 * i) * 80 + (2 * b + h) * 16) = o; }
;     }
;     asm volatile("s_waitcnt lgkmcnt(0)" ::: "memory");
; #pragma unroll
;     for (int qd = 0; qd < 8; ++qd) {
;         const int rho = 16 * qd + (lane >> 2), piece = lane & 3;
;         const u32x4 o = *(const LAS u32x4*)(scr + rho * 80 + piece * 16);
;         const int nl = 4 * (rho & 31) + (rho >> 5);
;         *(u32x4*)(WT + (size_t)(n0 + nl) * K + k0 + piece * 16) = o; }
;     asm volatile("s_waitcnt lgkmcnt(0)" ::: "memory");
	v_mul_f32_e32 v12, 0x43800000, v28
	v_cvt_pk_fp8_f32 v123, v8, v12 op_sel:[0,0,1]
	v_mul_f32_e32 v0, 0x43800000, v33
	v_mul_f32_e32 v4, 0x43800000, v37
	v_mul_f32_e32 v8, 0x43800000, v49
	ds_write_b128 v117, v[120:123] offset:32
	v_mov_b32_e32 v120, v153
	v_cvt_pk_fp8_f32 v120, v0, v4
	v_mul_f32_e32 v0, 0x43800000, v41
	v_mul_f32_e32 v4, 0x43800000, v45
	v_mov_b32_e32 v121, v153
	v_cvt_pk_fp8_f32 v121, v0, v4
	v_mul_f32_e32 v0, 0x43800000, v1
	v_mul_f32_e32 v1, 0x43800000, v5
	v_mov_b32_e32 v122, v153
	v_cvt_pk_fp8_f32 v122, v0, v1
	v_mul_f32_e32 v0, 0x43800000, v9
	v_mul_f32_e32 v1, 0x43800000, v13
	v_mov_b32_e32 v123, v153
	v_cvt_pk_fp8_f32 v123, v0, v1
	v_mul_f32_e32 v12, 0x43800000, v53
	v_mul_f32_e32 v4, 0x43800000, v17
	v_mul_f32_e32 v5, 0x43800000, v21
	v_cvt_pk_fp8_f32 v120, v8, v12 op_sel:[0,0,1]
	v_mul_f32_e32 v8, 0x43800000, v57
	v_mul_f32_e32 v12, 0x43800000, v61
	v_cvt_pk_fp8_f32 v122, v4, v5 op_sel:[0,0,1]
	v_mul_f32_e32 v4, 0x43800000, v25
	v_mul_f32_e32 v5, 0x43800000, v29
	v_cvt_pk_fp8_f32 v121, v8, v12 op_sel:[0,0,1]
	v_cvt_pk_fp8_f32 v123, v4, v5 op_sel:[0,0,1]
	v_mul_f32_e32 v0, 0x43800000, v34
	v_mul_f32_e32 v1, 0x43800000, v38
	v_mul_f32_e32 v4, 0x43800000, v50
	ds_write_b128 v117, v[120:123] offset:2592
	v_mov_b32_e32 v120, v153
	v_cvt_pk_fp8_f32 v120, v0, v1
	v_mul_f32_e32 v0, 0x43800000, v42
	v_mul_f32_e32 v1, 0x43800000, v46
	v_mov_b32_e32 v121, v153
	v_cvt_pk_fp8_f32 v121, v0, v1
	v_mul_f32_e32 v0, 0x43800000, v2
	v_mul_f32_e32 v1, 0x43800000, v6
	v_mov_b32_e32 v122, v153
	v_cvt_pk_fp8_f32 v122, v0, v1
	v_mul_f32_e32 v0, 0x43800000, v10
	v_mul_f32_e32 v1, 0x43800000, v14
	v_mov_b32_e32 v123, v153
	v_mul_f32_e32 v5, 0x43800000, v54
	v_cvt_pk_fp8_f32 v123, v0, v1
	v_cvt_pk_fp8_f32 v120, v4, v5 op_sel:[0,0,1]
	v_mul_f32_e32 v4, 0x43800000, v58
	v_mul_f32_e32 v5, 0x43800000, v62
	v_cvt_pk_fp8_f32 v121, v4, v5 op_sel:[0,0,1]
	v_mul_f32_e32 v2, 0x43800000, v18
	v_mul_f32_e32 v4, 0x43800000, v22
	v_cvt_pk_fp8_f32 v122, v2, v4 op_sel:[0,0,1]
	v_mul_f32_e32 v2, 0x43800000, v26
	v_mul_f32_e32 v4, 0x43800000, v30
	v_cvt_pk_fp8_f32 v123, v2, v4 op_sel:[0,0,1]
	v_mul_f32_e32 v1, 0x43800000, v35
	v_mul_f32_e32 v2, 0x43800000, v39
	v_mov_b32_e32 v0, v153
	v_cvt_pk_fp8_f32 v0, v1, v2
	v_mul_f32_e32 v4, 0x43800000, v51
	v_mul_f32_e32 v5, 0x43800000, v55
	v_mul_f32_e32 v2, 0x43800000, v43
	v_cvt_pk_fp8_f32 v0, v4, v5 op_sel:[0,0,1]
	v_mul_f32_e32 v4, 0x43800000, v47
	v_mov_b32_e32 v1, v153
	v_cvt_pk_fp8_f32 v1, v2, v4
	v_mul_f32_e32 v3, 0x43800000, v3
	v_mul_f32_e32 v4, 0x43800000, v7
	v_mov_b32_e32 v2, v153
	v_cvt_pk_fp8_f32 v2, v3, v4
	v_mul_f32_e32 v5, 0x43800000, v59
	v_mul_f32_e32 v6, 0x43800000, v63
	v_cvt_pk_fp8_f32 v1, v5, v6 op_sel:[0,0,1]
	v_mul_f32_e32 v5, 0x43800000, v19
	v_mul_f32_e32 v6, 0x43800000, v23
	v_cvt_pk_fp8_f32 v2, v5, v6 op_sel:[0,0,1]
	v_mul_f32_e32 v4, 0x43800000, v11
	v_mul_f32_e32 v5, 0x43800000, v15
	v_mov_b32_e32 v3, v153
	v_cvt_pk_fp8_f32 v3, v4, v5
	v_mul_f32_e32 v6, 0x43800000, v27
	v_mul_f32_e32 v7, 0x43800000, v31
	ds_write_b128 v117, v[120:123] offset:5152
	v_cvt_pk_fp8_f32 v3, v6, v7 op_sel:[0,0,1]
	v_add_u32_e32 v6, s0, v104
	v_ashrrev_i32_e32 v7, 31, v6
	v_lshl_add_u64 v[4:5], s[2:3], 0, v[66:67]
	ds_write_b128 v117, v[0:3] offset:7712
	s_waitcnt lgkmcnt(0)
	ds_read_b128 v[0:3], v118
	v_lshlrev_b64 v[6:7], 10, v[6:7]
	v_lshl_add_u64 v[6:7], v[4:5], 0, v[6:7]
	s_waitcnt lgkmcnt(0)
	global_store_dwordx4 v[6:7], v[0:3], off
	ds_read_b128 v[0:3], v118 offset:1280
	v_add_u32_e32 v6, s0, v105
	v_ashrrev_i32_e32 v7, 31, v6
	v_lshlrev_b64 v[6:7], 10, v[6:7]
	v_lshl_add_u64 v[6:7], v[4:5], 0, v[6:7]
	s_waitcnt lgkmcnt(0)
	global_store_dwordx4 v[6:7], v[0:3], off
	ds_read_b128 v[0:3], v118 offset:2560
	v_add_u32_e32 v6, s0, v106
	v_ashrrev_i32_e32 v7, 31, v6
	v_lshlrev_b64 v[6:7], 10, v[6:7]
	v_lshl_add_u64 v[6:7], v[4:5], 0, v[6:7]
	s_waitcnt lgkmcnt(0)
	global_store_dwordx4 v[6:7], v[0:3], off
	ds_read_b128 v[0:3], v118 offset:3840
	v_add_u32_e32 v6, s0, v107
	v_ashrrev_i32_e32 v7, 31, v6
	v_lshlrev_b64 v[6:7], 10, v[6:7]
	v_lshl_add_u64 v[6:7], v[4:5], 0, v[6:7]
	s_waitcnt lgkmcnt(0)
	global_store_dwordx4 v[6:7], v[0:3], off
	ds_read_b128 v[0:3], v118 offset:5120
	v_add_u32_e32 v6, s0, v108
	v_ashrrev_i32_e32 v7, 31, v6
	v_lshlrev_b64 v[6:7], 10, v[6:7]
	v_lshl_add_u64 v[6:7], v[4:5], 0, v[6:7]
	s_waitcnt lgkmcnt(0)
	global_store_dwordx4 v[6:7], v[0:3], off
	ds_read_b128 v[0:3], v118 offset:6400
	v_add_u32_e32 v6, s0, v109
	v_ashrrev_i32_e32 v7, 31, v6
	v_lshlrev_b64 v[6:7], 10, v[6:7]
	v_lshl_add_u64 v[6:7], v[4:5], 0, v[6:7]
	s_waitcnt lgkmcnt(0)
	global_store_dwordx4 v[6:7], v[0:3], off
	ds_read_b128 v[0:3], v118 offset:7680
	v_add_u32_e32 v6, s0, v110
	v_ashrrev_i32_e32 v7, 31, v6
	v_lshlrev_b64 v[6:7], 10, v[6:7]
	v_lshl_add_u64 v[6:7], v[4:5], 0, v[6:7]
	s_waitcnt lgkmcnt(0)
	global_store_dwordx4 v[6:7], v[0:3], off
	ds_read_b128 v[0:3], v118 offset:8960
	v_add_u32_e32 v6, s0, v111
	v_ashrrev_i32_e32 v7, 31, v6
	v_lshlrev_b64 v[6:7], 10, v[6:7]
	v_lshl_add_u64 v[4:5], v[4:5], 0, v[6:7]
	s_waitcnt lgkmcnt(0)
	global_store_dwordx4 v[4:5], v[0:3], off
	s_waitcnt lgkmcnt(0)
	s_mov_b64 s[0:1], 0
; #define LAS __attribute__((address_space(3)))
; __device__ __forceinline__ unsigned pk4_fp8(float x0, float x1, float x2, float x3) { int w = 0; w = __builtin_amdgcn_cvt_pk_fp8_f32(x0, x1, w, false); w = __builtin_amdgcn_cvt_pk_fp8_f32(x2, x3, w, true); return (unsigned)w; }
; __device__ __forceinline__ void transpose_item_fp8w(const float* W, int K, int N, unsigned char* WT, float q, LAS unsigned char* scr, int item, int lane) {
;     const int nblk = N / 128, kb = item / nblk, nb = item % nblk, k0 = 64 * kb, n0 = 128 * nb;
;     const int l5 = lane & 31, h = lane >> 5;
;     const float* src = W + (size_t)(k0 + 16 * h) * N + n0 + 4 * l5;
; #pragma unroll
;     for (int b = 0; b < 2; ++b) {
;         f32x4 x[16];
; #pragma unroll
;         for (int s_ = 0; s_ < 16; ++s_) x[s_] = *(const f32x4*)(src + (size_t)(32 * b + s_) * N);
; #pragma unroll
;         for (int i = 0; i < 4; ++i) {
;             u32x4 o;
;             o.x = pk4_fp8(x[0][i] * q, x[1][i] * q, x[2][i] * q, x[3][i] * q); o.y = pk4_fp8(x[4][i] * q, x[5][i] * q, x[6][i] * q, x[7][i] * q);
;             o.z = pk4_fp8(x[8][i] * q, x[9][i] * q, x[10][i] * q, x[11][i] * q); o.w = pk4_fp8(x[12][i] * q, x[13][i] * q, x[14][i] * q, x[15][i] * q);
;             *(LAS u32x4*)(scr + (l5 + 32 * i) * 80 + (2 * b + h) * 16) = o; }
.LBB0_668:
	s_andn2_b64 vcc, exec, s[0:1]
	s_cbranch_vccnz .LBB0_670
	s_add_i32 s4, s5, 0xfffff910
	v_readlane_b32 s2, v253, 32
	s_lshr_b32 s0, s4, 8
	v_readlane_b32 s3, v253, 33
	s_mov_b32 s9, s3
	s_add_i32 s8, s0, s56
	v_readlane_b32 s40, v253, 58
	s_lshl_b64 s[0:1], s[8:9], 23
	v_readlane_b32 s50, v254, 4
	v_readlane_b32 s51, v254, 5
	s_add_u32 s2, s50, s0
	s_addc_u32 s3, s51, s1
	s_lshl_b64 s[6:7], s[8:9], 21
	v_readlane_b32 s0, v246, 15
	s_add_u32 s1, s0, s6
	v_readlane_b32 s0, v246, 16
	s_addc_u32 s6, s0, s7
	s_lshl_b32 s0, s4, 6
	s_and_b32 s7, s0, 0x3c0
	v_add_u32_e32 v0, s7, v99
	s_lshl_b32 s0, s4, 3
	v_ashrrev_i32_e32 v1, 31, v0
	s_and_b32 s0, s0, 0x780
	v_lshlrev_b64 v[0:1], 13, v[0:1]
	v_lshl_add_u64 v[0:1], s[2:3], 0, v[0:1]
	s_lshl_b32 s8, s0, 2
	s_mov_b32 s3, s9
	v_readlane_b32 s41, v253, 59
	v_readlane_b32 s42, v253, 60
	v_readlane_b32 s43, v253, 61
	v_readlane_b32 s44, v253, 62
	v_readlane_b32 s45, v253, 63
	v_writelane_b32 v253, s2, 32
	v_lshl_add_u64 v[0:1], v[0:1], 0, s[8:9]
	v_lshl_add_u64 v[60:61], v[0:1], 0, v[152:153]
	v_writelane_b32 v253, s3, 33
	s_movk_i32 s2, 0x2000
	v_add_co_u32_e32 v4, vcc, s2, v60
	s_movk_i32 s2, 0x4000
	s_nop 0
	v_addc_co_u32_e32 v5, vcc, 0, v61, vcc
	v_add_co_u32_e32 v8, vcc, s2, v60
	s_movk_i32 s2, 0x6000
	s_nop 0
	v_addc_co_u32_e32 v9, vcc, 0, v61, vcc
	v_add_co_u32_e32 v12, vcc, s2, v60
	s_mov_b32 s2, 0x8000
	s_nop 0
	v_addc_co_u32_e32 v13, vcc, 0, v61, vcc
	v_add_co_u32_e32 v16, vcc, s2, v60
	s_mov_b32 s2, 0xa000
	s_nop 0
	v_addc_co_u32_e32 v17, vcc, 0, v61, vcc
	v_add_co_u32_e32 v20, vcc, s2, v60
	s_mov_b32 s2, 0xc000
	s_nop 0
	v_addc_co_u32_e32 v21, vcc, 0, v61, vcc
	v_add_co_u32_e32 v24, vcc, s2, v60
	s_mov_b32 s2, 0xe000
	s_nop 0
	v_addc_co_u32_e32 v25, vcc, 0, v61, vcc
	v_add_co_u32_e32 v28, vcc, s2, v60
	s_mov_b32 s2, 0x10000
	s_nop 0
	v_addc_co_u32_e32 v29, vcc, 0, v61, vcc
	v_add_co_u32_e32 v32, vcc, s2, v60
	s_mov_b32 s2, 0x12000
	s_nop 0
	v_addc_co_u32_e32 v33, vcc, 0, v61, vcc
	v_add_co_u32_e32 v36, vcc, s2, v60
	s_mov_b32 s2, 0x14000
	s_nop 0
	v_addc_co_u32_e32 v37, vcc, 0, v61, vcc
	v_add_co_u32_e32 v40, vcc, s2, v60
	s_mov_b32 s2, 0x16000
	s_nop 0
	v_addc_co_u32_e32 v41, vcc, 0, v61, vcc
	v_add_co_u32_e32 v44, vcc, s2, v60
	s_mov_b32 s2, 0x18000
	s_nop 0
	v_addc_co_u32_e32 v45, vcc, 0, v61, vcc
	v_add_co_u32_e32 v48, vcc, s2, v60
	global_load_dwordx4 v[0:3], v[60:61], off
	s_nop 0
	v_addc_co_u32_e32 v49, vcc, 0, v61, vcc
	global_load_dwordx4 v[4:7], v[4:5], off
	s_mov_b32 s2, 0x1a000
	global_load_dwordx4 v[12:15], v[12:13], off
	v_add_co_u32_e32 v52, vcc, s2, v60
	global_load_dwordx4 v[16:19], v[16:17], off
	s_nop 0
	v_addc_co_u32_e32 v53, vcc, 0, v61, vcc
	global_load_dwordx4 v[20:23], v[20:21], off
	s_mov_b32 s2, 0x1c000
	global_load_dwordx4 v[28:31], v[28:29], off
	v_add_co_u32_e32 v56, vcc, s2, v60
	global_load_dwordx4 v[32:35], v[32:33], off
	s_nop 0
	v_addc_co_u32_e32 v57, vcc, 0, v61, vcc
	global_load_dwordx4 v[36:39], v[36:37], off
	s_mov_b32 s2, 0x1e000
	global_load_dwordx4 v[44:47], v[44:45], off
	v_add_co_u32_e32 v62, vcc, s2, v60
	global_load_dwordx4 v[48:51], v[48:49], off
	s_nop 0
	v_addc_co_u32_e32 v63, vcc, 0, v61, vcc
	global_load_dwordx4 v[52:55], v[52:53], off
	v_mov_b32_e32 v124, v153
	global_load_dwordx4 v[8:11], v[8:9], off
	v_mov_b32_e32 v125, v153
	global_load_dwordx4 v[24:27], v[24:25], off
	v_mov_b32_e32 v126, v153
	global_load_dwordx4 v[40:43], v[40:41], off
	v_mov_b32_e32 v127, v153
	global_load_dwordx4 v[56:59], v[56:57], off
	s_mov_b32 s2, 0x40000
	global_load_dwordx4 v[120:123], v[62:63], off
	v_readlane_b32 s46, v254, 0
	v_readlane_b32 s47, v254, 1
	v_readlane_b32 s48, v254, 2
	v_readlane_b32 s49, v254, 3
	v_readlane_b32 s52, v254, 6
	v_readlane_b32 s53, v254, 7
	v_readlane_b32 s54, v254, 8
	v_readlane_b32 s55, v254, 9
	s_waitcnt vmcnt(0)
	v_mul_f32_e32 v0, 0x43000000, v0
	v_mul_f32_e32 v4, 0x43000000, v4
	v_cvt_pk_fp8_f32 v124, v0, v4
	v_mul_f32_e32 v12, 0x43000000, v12
	v_mul_f32_e32 v0, 0x43000000, v16
	v_mul_f32_e32 v4, 0x43000000, v20
	v_cvt_pk_fp8_f32 v125, v0, v4
	v_mul_f32_e32 v0, 0x43000000, v32
	v_mul_f32_e32 v4, 0x43000000, v36
	v_cvt_pk_fp8_f32 v126, v0, v4
	v_mul_f32_e32 v0, 0x43000000, v48
	v_mul_f32_e32 v4, 0x43000000, v52
	v_cvt_pk_fp8_f32 v127, v0, v4
	v_mul_f32_e32 v8, 0x43000000, v8
	v_cvt_pk_fp8_f32 v124, v8, v12 op_sel:[0,0,1]
	v_mul_f32_e32 v8, 0x43000000, v24
	v_mul_f32_e32 v12, 0x43000000, v28
	v_cvt_pk_fp8_f32 v125, v8, v12 op_sel:[0,0,1]
	v_mul_f32_e32 v8, 0x43000000, v40
	v_mul_f32_e32 v12, 0x43000000, v44
	v_cvt_pk_fp8_f32 v126, v8, v12 op_sel:[0,0,1]
	v_mul_f32_e32 v8, 0x43000000, v56
	v_mul_f32_e32 v12, 0x43000000, v120
	v_cvt_pk_fp8_f32 v127, v8, v12 op_sel:[0,0,1]
	v_mul_f32_e32 v0, 0x43000000, v1
	v_mul_f32_e32 v1, 0x43000000, v5
	v_mul_f32_e32 v4, 0x43000000, v9
	ds_write_b128 v117, v[124:127]
	v_mov_b32_e32 v124, v153
	v_cvt_pk_fp8_f32 v124, v0, v1
	v_mul_f32_e32 v0, 0x43000000, v17
	v_mul_f32_e32 v1, 0x43000000, v21
	v_mov_b32_e32 v125, v153
	v_cvt_pk_fp8_f32 v125, v0, v1
	v_mul_f32_e32 v0, 0x43000000, v33
	v_mul_f32_e32 v1, 0x43000000, v37
	v_mov_b32_e32 v126, v153
	v_cvt_pk_fp8_f32 v126, v0, v1
	v_mul_f32_e32 v0, 0x43000000, v49
	v_mul_f32_e32 v1, 0x43000000, v53
	v_mov_b32_e32 v127, v153
	v_mul_f32_e32 v5, 0x43000000, v13
	v_cvt_pk_fp8_f32 v127, v0, v1
	v_cvt_pk_fp8_f32 v124, v4, v5 op_sel:[0,0,1]
	v_mul_f32_e32 v4, 0x43000000, v25
	v_mul_f32_e32 v5, 0x43000000, v29
	v_cvt_pk_fp8_f32 v125, v4, v5 op_sel:[0,0,1]
	v_mul_f32_e32 v4, 0x43000000, v41
	v_mul_f32_e32 v5, 0x43000000, v45
	v_cvt_pk_fp8_f32 v126, v4, v5 op_sel:[0,0,1]
	v_mul_f32_e32 v4, 0x43000000, v57
	v_mul_f32_e32 v5, 0x43000000, v121
; #define LAS __attribute__((address_space(3)))
; __device__ __forceinline__ unsigned pk4_fp8(float x0, float x1, float x2, float x3) { int w = 0; w = __builtin_amdgcn_cvt_pk_fp8_f32(x0, x1, w, false); w = __builtin_amdgcn_cvt_pk_fp8_f32(x2, x3, w, true); return (unsigned)w; }
; __device__ __forceinline__ void transpose_item_fp8w(const float* W, int K, int N, unsigned char* WT, float q, LAS unsigned char* scr, int item, int lane) {
;     ...
;     for (int b = 0; b < 2; ++b) {
;         f32x4 x[16];
; #pragma unroll
;         for (int s_ = 0; s_ < 16; ++s_) x[s_] = *(const f32x4*)(src + (size_t)(32 * b + s_) * N);
; #pragma unroll
;         for (int i = 0; i < 4; ++i) {
;             u32x4 o;
;             o.x = pk4_fp8(x[0][i] * q, x[1][i] * q, x[2][i] * q, x[3][i] * q); o.y = pk4_fp8(x[4][i] * q, x[5][i] * q, x[6][i] * q, x[7][i] * q);
;             o.z = pk4_fp8(x[8][i] * q, x[9][i] * q, x[10][i] * q, x[11][i] * q); o.w = pk4_fp8(x[12][i] * q, x[13][i] * q, x[14][i] * q, x[15][i] * q);
;             *(LAS u32x4*)(scr + (l5 + 32 * i) * 80 + (2 * b + h) * 16) = o; }
;     }
;     asm volatile("s_waitcnt lgkmcnt(0)" ::: "memory");
; #pragma unroll
;     for (int qd = 0; qd < 8; ++qd) {
;         const int rho = 16 * qd + (lane >> 2), piece = lane & 3;
;         const u32x4 o = *(const LAS u32x4*)(scr + rho * 80 + piece * 16);
;         const int nl = 4 * (rho & 31) + (rho >> 5);
;         *(u32x4*)(WT + (size_t)(n0 + nl) * K + k0 + piece * 16) = o; }
	v_cvt_pk_fp8_f32 v127, v4, v5 op_sel:[0,0,1]
	v_mul_f32_e32 v0, 0x43000000, v2
	v_mul_f32_e32 v1, 0x43000000, v6
	v_mul_f32_e32 v2, 0x43000000, v10
	ds_write_b128 v117, v[124:127] offset:2560
	v_mov_b32_e32 v124, v153
	v_cvt_pk_fp8_f32 v124, v0, v1
	v_mul_f32_e32 v0, 0x43000000, v18
	v_mul_f32_e32 v1, 0x43000000, v22
	v_mov_b32_e32 v125, v153
	v_cvt_pk_fp8_f32 v125, v0, v1
	v_mul_f32_e32 v0, 0x43000000, v34
	v_mul_f32_e32 v1, 0x43000000, v38
	v_mov_b32_e32 v126, v153
	v_cvt_pk_fp8_f32 v126, v0, v1
	v_mul_f32_e32 v0, 0x43000000, v50
	v_mul_f32_e32 v1, 0x43000000, v54
	v_mov_b32_e32 v127, v153
	v_mul_f32_e32 v4, 0x43000000, v14
	v_cvt_pk_fp8_f32 v127, v0, v1
	v_cvt_pk_fp8_f32 v124, v2, v4 op_sel:[0,0,1]
	v_mul_f32_e32 v2, 0x43000000, v26
	v_mul_f32_e32 v4, 0x43000000, v30
	v_cvt_pk_fp8_f32 v125, v2, v4 op_sel:[0,0,1]
	v_mul_f32_e32 v2, 0x43000000, v42
	v_mul_f32_e32 v4, 0x43000000, v46
	v_cvt_pk_fp8_f32 v126, v2, v4 op_sel:[0,0,1]
	v_mul_f32_e32 v2, 0x43000000, v58
	v_mul_f32_e32 v4, 0x43000000, v122
	v_cvt_pk_fp8_f32 v127, v2, v4 op_sel:[0,0,1]
	v_mul_f32_e32 v1, 0x43000000, v3
	v_mul_f32_e32 v2, 0x43000000, v7
	v_mov_b32_e32 v0, v153
	v_cvt_pk_fp8_f32 v0, v1, v2
	v_mul_f32_e32 v3, 0x43000000, v11
	v_mul_f32_e32 v4, 0x43000000, v15
	v_mul_f32_e32 v2, 0x43000000, v19
	v_cvt_pk_fp8_f32 v0, v3, v4 op_sel:[0,0,1]
	v_mul_f32_e32 v3, 0x43000000, v23
	v_mov_b32_e32 v1, v153
	v_cvt_pk_fp8_f32 v1, v2, v3
	v_mul_f32_e32 v4, 0x43000000, v27
	v_mul_f32_e32 v5, 0x43000000, v31
	v_mul_f32_e32 v3, 0x43000000, v35
	v_cvt_pk_fp8_f32 v1, v4, v5 op_sel:[0,0,1]
	v_mul_f32_e32 v4, 0x43000000, v39
	v_mov_b32_e32 v2, v153
	v_cvt_pk_fp8_f32 v2, v3, v4
	v_mul_f32_e32 v5, 0x43000000, v43
	v_mul_f32_e32 v6, 0x43000000, v47
	v_mul_f32_e32 v4, 0x43000000, v51
	v_cvt_pk_fp8_f32 v2, v5, v6 op_sel:[0,0,1]
	v_mul_f32_e32 v5, 0x43000000, v55
	v_mov_b32_e32 v3, v153
	v_cvt_pk_fp8_f32 v3, v4, v5
	v_mul_f32_e32 v6, 0x43000000, v59
	v_mul_f32_e32 v7, 0x43000000, v123
	v_mov_b32_e32 v120, v153
	v_cvt_pk_fp8_f32 v3, v6, v7 op_sel:[0,0,1]
	v_mov_b32_e32 v121, v153
	v_mov_b32_e32 v122, v153
	v_mov_b32_e32 v123, v153
	ds_write_b128 v117, v[0:3] offset:7680
	v_add_co_u32_e32 v0, vcc, s2, v60
	s_mov_b32 s2, 0x42000
	s_nop 0
	v_addc_co_u32_e32 v1, vcc, 0, v61, vcc
	v_add_co_u32_e32 v4, vcc, s2, v60
	s_mov_b32 s2, 0x44000
	s_nop 0
	v_addc_co_u32_e32 v5, vcc, 0, v61, vcc
	v_add_co_u32_e32 v8, vcc, s2, v60
	s_mov_b32 s2, 0x46000
	s_nop 0
	v_addc_co_u32_e32 v9, vcc, 0, v61, vcc
	v_add_co_u32_e32 v12, vcc, s2, v60
	s_mov_b32 s2, 0x48000
	s_nop 0
	v_addc_co_u32_e32 v13, vcc, 0, v61, vcc
	global_load_dwordx4 v[8:11], v[8:9], off
	ds_write_b128 v117, v[124:127] offset:5120
	global_load_dwordx4 v[16:19], v[12:13], off
	v_add_co_u32_e32 v12, vcc, s2, v60
	s_mov_b32 s2, 0x4a000
	s_nop 0
	v_addc_co_u32_e32 v13, vcc, 0, v61, vcc
	v_add_co_u32_e32 v20, vcc, s2, v60
	s_mov_b32 s2, 0x4c000
	s_nop 0
	v_addc_co_u32_e32 v21, vcc, 0, v61, vcc
	global_load_dwordx4 v[12:15], v[12:13], off
	s_waitcnt vmcnt(0)
	v_mul_f32_e32 v8, 0x43000000, v8
	global_load_dwordx4 v[24:27], v[20:21], off
	v_add_co_u32_e32 v20, vcc, s2, v60
	s_mov_b32 s2, 0x4e000
	s_nop 0
	v_addc_co_u32_e32 v21, vcc, 0, v61, vcc
	global_load_dwordx4 v[28:31], v[20:21], off
	v_add_co_u32_e32 v20, vcc, s2, v60
	s_mov_b32 s2, 0x50000
	s_nop 0
	v_addc_co_u32_e32 v21, vcc, 0, v61, vcc
	global_load_dwordx4 v[40:43], v[20:21], off
	v_add_co_u32_e32 v20, vcc, s2, v60
	s_mov_b32 s2, 0x52000
	s_nop 0
	v_addc_co_u32_e32 v21, vcc, 0, v61, vcc
	v_add_co_u32_e32 v32, vcc, s2, v60
	s_mov_b32 s2, 0x54000
	s_nop 0
	v_addc_co_u32_e32 v33, vcc, 0, v61, vcc
	v_add_co_u32_e32 v36, vcc, s2, v60
	s_mov_b32 s2, 0x56000
	s_nop 0
	v_addc_co_u32_e32 v37, vcc, 0, v61, vcc
	v_add_co_u32_e32 v44, vcc, s2, v60
	s_mov_b32 s2, 0x58000
	s_nop 0
	v_addc_co_u32_e32 v45, vcc, 0, v61, vcc
	global_load_dwordx4 v[36:39], v[36:37], off
	s_waitcnt vmcnt(5)
	v_mul_f32_e32 v16, 0x43000000, v16
	global_load_dwordx4 v[48:51], v[44:45], off
	v_add_co_u32_e32 v44, vcc, s2, v60
	global_load_dwordx4 v[0:3], v[0:1], off
	s_nop 0
	v_addc_co_u32_e32 v45, vcc, 0, v61, vcc
	global_load_dwordx4 v[4:7], v[4:5], off
	s_mov_b32 s2, 0x5a000
	v_add_co_u32_e32 v52, vcc, s2, v60
	global_load_dwordx4 v[20:23], v[20:21], off
	s_nop 0
	v_addc_co_u32_e32 v53, vcc, 0, v61, vcc
	global_load_dwordx4 v[32:35], v[32:33], off
	s_mov_b32 s2, 0x5c000
	global_load_dwordx4 v[44:47], v[44:45], off
	v_add_co_u32_e32 v56, vcc, s2, v60
	global_load_dwordx4 v[52:55], v[52:53], off
	s_nop 0
	v_addc_co_u32_e32 v57, vcc, 0, v61, vcc
	s_mov_b32 s2, 0x5e000
	v_add_co_u32_e32 v60, vcc, s2, v60
	global_load_dwordx4 v[56:59], v[56:57], off
	s_nop 0
	v_addc_co_u32_e32 v61, vcc, 0, v61, vcc
	global_load_dwordx4 v[60:63], v[60:61], off
	s_add_u32 s2, s1, s7
	s_addc_u32 s3, s6, 0
	s_waitcnt vmcnt(0)
	v_mul_f32_e32 v0, 0x43000000, v0
	s_waitcnt vmcnt(6)
	v_mul_f32_e32 v4, 0x43000000, v4
	v_cvt_pk_fp8_f32 v120, v0, v4
	v_mul_f32_e32 v0, 0x43000000, v12
	v_mul_f32_e32 v4, 0x43000000, v24
	v_cvt_pk_fp8_f32 v121, v0, v4
	s_waitcnt vmcnt(5)
	v_mul_f32_e32 v0, 0x43000000, v20
	v_cvt_pk_fp8_f32 v120, v8, v16 op_sel:[0,0,1]
	s_waitcnt vmcnt(4)
	v_mul_f32_e32 v4, 0x43000000, v32
	v_cvt_pk_fp8_f32 v122, v0, v4
	s_waitcnt vmcnt(3)
	v_mul_f32_e32 v0, 0x43000000, v44
	v_mul_f32_e32 v8, 0x43000000, v28
	v_mul_f32_e32 v12, 0x43000000, v40
	s_waitcnt vmcnt(2)
; #define LAS __attribute__((address_space(3)))
; __device__ __forceinline__ unsigned pk4_fp8(float x0, float x1, float x2, float x3) { int w = 0; w = __builtin_amdgcn_cvt_pk_fp8_f32(x0, x1, w, false); w = __builtin_amdgcn_cvt_pk_fp8_f32(x2, x3, w, true); return (unsigned)w; }
; __device__ __forceinline__ void transpose_item_fp8w(const float* W, int K, int N, unsigned char* WT, float q, LAS unsigned char* scr, int item, int lane) {
;     ...
;         for (int i = 0; i < 4; ++i) {
;             u32x4 o;
;             o.x = pk4_fp8(x[0][i] * q, x[1][i] * q, x[2][i] * q, x[3][i] * q); o.y = pk4_fp8(x[4][i] * q, x[5][i] * q, x[6][i] * q, x[7][i] * q);
;             o.z = pk4_fp8(x[8][i] * q, x[9][i] * q, x[10][i] * q, x[11][i] * q); o.w = pk4_fp8(x[12][i] * q, x[13][i] * q, x[14][i] * q, x[15][i] * q);
;             *(LAS u32x4*)(scr + (l5 + 32 * i) * 80 + (2 * b + h) * 16) = o; }
;     }
;     asm volatile("s_waitcnt lgkmcnt(0)" ::: "memory");
; #pragma unroll
;     for (int qd = 0; qd < 8; ++qd) {
;         const int rho = 16 * qd + (lane >> 2), piece = lane & 3;
;         const u32x4 o = *(const LAS u32x4*)(scr + rho * 80 + piece * 16);
;         const int nl = 4 * (rho & 31) + (rho >> 5);
;         *(u32x4*)(WT + (size_t)(n0 + nl) * K + k0 + piece * 16) = o; }
;     asm volatile("s_waitcnt lgkmcnt(0)" ::: "memory");
	v_mul_f32_e32 v4, 0x43000000, v52
	v_cvt_pk_fp8_f32 v123, v0, v4
	v_cvt_pk_fp8_f32 v121, v8, v12 op_sel:[0,0,1]
	v_mul_f32_e32 v8, 0x43000000, v36
	v_mul_f32_e32 v12, 0x43000000, v48
	v_cvt_pk_fp8_f32 v122, v8, v12 op_sel:[0,0,1]
	s_waitcnt vmcnt(1)
	v_mul_f32_e32 v8, 0x43000000, v56
	v_mul_f32_e32 v0, 0x43000000, v1
	v_mul_f32_e32 v1, 0x43000000, v5
	s_waitcnt vmcnt(0)
	v_mul_f32_e32 v12, 0x43000000, v60
	v_cvt_pk_fp8_f32 v123, v8, v12 op_sel:[0,0,1]
	v_mul_f32_e32 v4, 0x43000000, v9
	v_mul_f32_e32 v5, 0x43000000, v17
	ds_write_b128 v117, v[120:123] offset:32
	v_mov_b32_e32 v120, v153
	v_cvt_pk_fp8_f32 v120, v0, v1
	v_mul_f32_e32 v0, 0x43000000, v13
	v_mul_f32_e32 v1, 0x43000000, v25
	v_mov_b32_e32 v121, v153
	v_cvt_pk_fp8_f32 v121, v0, v1
	v_mul_f32_e32 v0, 0x43000000, v21
	v_mul_f32_e32 v1, 0x43000000, v33
	v_mov_b32_e32 v122, v153
	v_cvt_pk_fp8_f32 v122, v0, v1
	v_mul_f32_e32 v0, 0x43000000, v45
	v_mul_f32_e32 v1, 0x43000000, v53
	v_mov_b32_e32 v123, v153
	v_cvt_pk_fp8_f32 v123, v0, v1
	v_cvt_pk_fp8_f32 v120, v4, v5 op_sel:[0,0,1]
	v_mul_f32_e32 v4, 0x43000000, v29
	v_mul_f32_e32 v5, 0x43000000, v41
	v_cvt_pk_fp8_f32 v121, v4, v5 op_sel:[0,0,1]
	v_mul_f32_e32 v4, 0x43000000, v37
	v_mul_f32_e32 v5, 0x43000000, v49
	v_cvt_pk_fp8_f32 v122, v4, v5 op_sel:[0,0,1]
	v_mul_f32_e32 v4, 0x43000000, v57
	v_mul_f32_e32 v5, 0x43000000, v61
	v_cvt_pk_fp8_f32 v123, v4, v5 op_sel:[0,0,1]
	v_mul_f32_e32 v0, 0x43000000, v2
	v_mul_f32_e32 v1, 0x43000000, v6
	v_mul_f32_e32 v2, 0x43000000, v10
	ds_write_b128 v117, v[120:123] offset:2592
	v_mov_b32_e32 v120, v153
	v_cvt_pk_fp8_f32 v120, v0, v1
	v_mul_f32_e32 v0, 0x43000000, v14
	v_mul_f32_e32 v1, 0x43000000, v26
	v_mov_b32_e32 v121, v153
	v_cvt_pk_fp8_f32 v121, v0, v1
	v_mul_f32_e32 v0, 0x43000000, v22
	v_mul_f32_e32 v1, 0x43000000, v34
	v_mov_b32_e32 v122, v153
	v_cvt_pk_fp8_f32 v122, v0, v1
	v_mul_f32_e32 v0, 0x43000000, v46
	v_mul_f32_e32 v1, 0x43000000, v54
	v_mov_b32_e32 v123, v153
	v_mul_f32_e32 v4, 0x43000000, v18
	v_cvt_pk_fp8_f32 v123, v0, v1
	v_cvt_pk_fp8_f32 v120, v2, v4 op_sel:[0,0,1]
	v_mul_f32_e32 v2, 0x43000000, v30
	v_mul_f32_e32 v4, 0x43000000, v42
	v_cvt_pk_fp8_f32 v121, v2, v4 op_sel:[0,0,1]
	v_mul_f32_e32 v2, 0x43000000, v38
	v_mul_f32_e32 v4, 0x43000000, v50
	v_cvt_pk_fp8_f32 v122, v2, v4 op_sel:[0,0,1]
	v_mul_f32_e32 v2, 0x43000000, v58
	v_mul_f32_e32 v4, 0x43000000, v62
	v_cvt_pk_fp8_f32 v123, v2, v4 op_sel:[0,0,1]
	v_mul_f32_e32 v1, 0x43000000, v3
	v_mul_f32_e32 v2, 0x43000000, v7
	v_mov_b32_e32 v0, v153
	v_cvt_pk_fp8_f32 v0, v1, v2
	v_mul_f32_e32 v3, 0x43000000, v11
	v_mul_f32_e32 v4, 0x43000000, v19
	v_mul_f32_e32 v2, 0x43000000, v15
	v_cvt_pk_fp8_f32 v0, v3, v4 op_sel:[0,0,1]
	v_mul_f32_e32 v3, 0x43000000, v27
	v_mov_b32_e32 v1, v153
	v_cvt_pk_fp8_f32 v1, v2, v3
	v_mul_f32_e32 v4, 0x43000000, v31
	v_mul_f32_e32 v5, 0x43000000, v43
	v_mul_f32_e32 v3, 0x43000000, v23
	v_cvt_pk_fp8_f32 v1, v4, v5 op_sel:[0,0,1]
	v_mul_f32_e32 v4, 0x43000000, v35
	v_mov_b32_e32 v2, v153
	v_cvt_pk_fp8_f32 v2, v3, v4
	v_mul_f32_e32 v5, 0x43000000, v39
	v_mul_f32_e32 v6, 0x43000000, v51
	v_mul_f32_e32 v4, 0x43000000, v47
	v_cvt_pk_fp8_f32 v2, v5, v6 op_sel:[0,0,1]
	v_mul_f32_e32 v5, 0x43000000, v55
	v_mov_b32_e32 v3, v153
	v_cvt_pk_fp8_f32 v3, v4, v5
	v_mul_f32_e32 v6, 0x43000000, v59
	v_mul_f32_e32 v7, 0x43000000, v63
	ds_write_b128 v117, v[120:123] offset:5152
	v_cvt_pk_fp8_f32 v3, v6, v7 op_sel:[0,0,1]
	v_add_u32_e32 v6, s0, v104
	v_ashrrev_i32_e32 v7, 31, v6
	v_lshl_add_u64 v[4:5], s[2:3], 0, v[66:67]
	ds_write_b128 v117, v[0:3] offset:7712
	s_waitcnt lgkmcnt(0)
	ds_read_b128 v[0:3], v118
	v_lshlrev_b64 v[6:7], 10, v[6:7]
	v_lshl_add_u64 v[6:7], v[4:5], 0, v[6:7]
	s_waitcnt lgkmcnt(0)
	global_store_dwordx4 v[6:7], v[0:3], off
	ds_read_b128 v[0:3], v118 offset:1280
	v_add_u32_e32 v6, s0, v105
	v_ashrrev_i32_e32 v7, 31, v6
	v_lshlrev_b64 v[6:7], 10, v[6:7]
	v_lshl_add_u64 v[6:7], v[4:5], 0, v[6:7]
	s_waitcnt lgkmcnt(0)
	global_store_dwordx4 v[6:7], v[0:3], off
	ds_read_b128 v[0:3], v118 offset:2560
	v_add_u32_e32 v6, s0, v106
	v_ashrrev_i32_e32 v7, 31, v6
	v_lshlrev_b64 v[6:7], 10, v[6:7]
	v_lshl_add_u64 v[6:7], v[4:5], 0, v[6:7]
	s_waitcnt lgkmcnt(0)
	global_store_dwordx4 v[6:7], v[0:3], off
	ds_read_b128 v[0:3], v118 offset:3840
	v_add_u32_e32 v6, s0, v107
	v_ashrrev_i32_e32 v7, 31, v6
	v_lshlrev_b64 v[6:7], 10, v[6:7]
	v_lshl_add_u64 v[6:7], v[4:5], 0, v[6:7]
	s_waitcnt lgkmcnt(0)
	global_store_dwordx4 v[6:7], v[0:3], off
	ds_read_b128 v[0:3], v118 offset:5120
	v_add_u32_e32 v6, s0, v108
	v_ashrrev_i32_e32 v7, 31, v6
	v_lshlrev_b64 v[6:7], 10, v[6:7]
	v_lshl_add_u64 v[6:7], v[4:5], 0, v[6:7]
	s_waitcnt lgkmcnt(0)
	global_store_dwordx4 v[6:7], v[0:3], off
	ds_read_b128 v[0:3], v118 offset:6400
	v_add_u32_e32 v6, s0, v109
	v_ashrrev_i32_e32 v7, 31, v6
	v_lshlrev_b64 v[6:7], 10, v[6:7]
	v_lshl_add_u64 v[6:7], v[4:5], 0, v[6:7]
	s_waitcnt lgkmcnt(0)
	global_store_dwordx4 v[6:7], v[0:3], off
	ds_read_b128 v[0:3], v118 offset:7680
	v_add_u32_e32 v6, s0, v110
	v_ashrrev_i32_e32 v7, 31, v6
	v_lshlrev_b64 v[6:7], 10, v[6:7]
	v_lshl_add_u64 v[6:7], v[4:5], 0, v[6:7]
	s_waitcnt lgkmcnt(0)
	global_store_dwordx4 v[6:7], v[0:3], off
	ds_read_b128 v[0:3], v118 offset:8960
	v_add_u32_e32 v6, s0, v111
	v_ashrrev_i32_e32 v7, 31, v6
	v_lshlrev_b64 v[6:7], 10, v[6:7]
	v_lshl_add_u64 v[4:5], v[4:5], 0, v[6:7]
	s_waitcnt lgkmcnt(0)
	global_store_dwordx4 v[4:5], v[0:3], off
	s_waitcnt lgkmcnt(0)
